# wt4 + GEMM K-loops: first-iteration phase-1/2 waits after an epilogue use vmcnt(8+S) (do not drain the epilogue stores) for QKV/in-proj/out-proj/down
# speedup vs baseline: 1.0227x; 1.0198x over previous
.LBB0_252:
	s_mov_b32 s99, 0
	v_add_u32_e32 v0, s24, v3
	s_movk_i32 s6, 0x400
	v_cmp_gt_i32_e32 vcc, s6, v0
	s_and_saveexec_b64 s[6:7], vcc
	s_mov_b64 s[12:13], 0x2000
	s_cbranch_execz .LBB0_255
	s_lshl_b32 s8, s8, 10
	v_readlane_b32 s10, v254, 49
	s_add_i32 s8, s8, 0
	v_ashrrev_i32_e32 v1, 31, v0
	v_readlane_b32 s11, v254, 50
	s_add_i32 s8, s8, 0x20000
	v_add_u32_e32 v2, 0xfffffe00, v0
	v_lshl_add_u64 v[0:1], v[0:1], 4, s[10:11]
	v_lshl_add_u32 v3, v3, 4, s8
	s_mov_b64 s[8:9], 0

.LBB0_261:
	s_add_u32 s8, s6, 0xfffe0080
	s_addc_u32 s9, s7, -1
	s_add_i32 s57, 0, 0x10000
	s_cmp_eq_u32 s56, 4
	s_cselect_b32 s9, s69, s9
	s_cselect_b32 s8, s68, s8
	v_add_u32_e32 v64, s57, v162
	s_cselect_b32 s21, s22, s49
	s_cselect_b32 s20, s23, s39
	s_add_i32 s62, 0, 0x14000
	ds_read_b128 v[130:133], v64
	ds_read_b128 v[134:137], v64 offset:1024
	ds_read_b128 v[138:141], v64 offset:2048
	ds_read_b128 v[142:145], v64 offset:3072
	v_add_u32_e32 v64, s62, v162
	ds_read_b128 v[146:149], v64
	ds_read_b128 v[150:153], v64 offset:1024
	ds_read_b128 v[164:167], v64 offset:2048
	ds_read_b128 v[168:171], v64 offset:3072
	v_mov_b32_e32 v64, v156
	ds_read_b128 v[172:175], v163
	ds_read_b128 v[176:179], v163 offset:1024
	ds_read_b128 v[180:183], v163 offset:2048
	ds_read_b128 v[184:187], v163 offset:3072
	ds_read_b128 v[188:191], v163 offset:4096
	ds_read_b128 v[192:195], v163 offset:5120
	ds_read_b128 v[196:199], v163 offset:6144
	ds_read_b128 v[200:203], v163 offset:7168
	s_add_i32 m0, s26, 0xc000
	s_nop 0
	global_load_lds_dwordx4 v64, s[6:7]
	v_mov_b32_e32 v64, v158
	s_add_i32 m0, s26, 0xe000
	s_nop 0
	global_load_lds_dwordx4 v64, s[6:7]
	s_cmp_eq_u32 s99, 0
	s_cbranch_scc1 .Lrw_q1_n
	s_waitcnt vmcnt(24)
	s_branch .Lrw_q1_d
.Lrw_q1_n:
	s_waitcnt vmcnt(8)
.Lrw_q1_d:
	s_waitcnt lgkmcnt(0)
	s_barrier
	s_setprio 1
	s_waitcnt lgkmcnt(0)
	v_mfma_f32_16x16x128_f8f6f4 v[126:129], v[130:137], v[172:179], v[126:129]
	v_mfma_f32_16x16x128_f8f6f4 v[122:125], v[138:145], v[172:179], v[122:125]
	v_mfma_f32_16x16x128_f8f6f4 v[110:113], v[130:137], v[180:187], v[110:113]
	v_mfma_f32_16x16x128_f8f6f4 v[106:109], v[138:145], v[180:187], v[106:109]
	v_mfma_f32_16x16x128_f8f6f4 v[204:207], v[130:137], v[188:195], v[94:97]
	v_mfma_f32_16x16x128_f8f6f4 v[208:211], v[138:145], v[188:195], v[90:93]
	v_mfma_f32_16x16x128_f8f6f4 v[212:215], v[130:137], v[196:203], v[78:81]
	v_mfma_f32_16x16x128_f8f6f4 v[216:219], v[138:145], v[196:203], v[74:77]
	s_setprio 0
	s_setprio 1
	v_mfma_f32_16x16x128_f8f6f4 v[118:121], v[146:153], v[172:179], v[118:121]
	v_mfma_f32_16x16x128_f8f6f4 v[114:117], v[164:171], v[172:179], v[114:117]
	v_mfma_f32_16x16x128_f8f6f4 v[102:105], v[146:153], v[180:187], v[102:105]
	v_mfma_f32_16x16x128_f8f6f4 v[98:101], v[164:171], v[180:187], v[98:101]
	v_mfma_f32_16x16x128_f8f6f4 v[172:175], v[146:153], v[188:195], v[86:89]
	v_mfma_f32_16x16x128_f8f6f4 v[176:179], v[164:171], v[188:195], v[82:85]
	v_mfma_f32_16x16x128_f8f6f4 v[180:183], v[146:153], v[196:203], v[70:73]
	v_mfma_f32_16x16x128_f8f6f4 v[184:187], v[164:171], v[196:203], v[66:69]
	s_setprio 0
	s_barrier
	v_mov_b32_e32 v64, v157
	s_add_i32 s57, s57, s25
	s_nop 2
	ds_read_b128 v[66:69], v163 offset:16384
	ds_read_b128 v[70:73], v163 offset:17408
	ds_read_b128 v[74:77], v163 offset:18432
	ds_read_b128 v[78:81], v163 offset:19456
	ds_read_b128 v[82:85], v163 offset:20480
	ds_read_b128 v[86:89], v163 offset:21504
	ds_read_b128 v[90:93], v163 offset:22528
	ds_read_b128 v[94:97], v163 offset:23552
	s_mov_b32 m0, s57
	s_nop 0
	global_load_lds_dwordx4 v64, s[20:21]
	v_mov_b32_e32 v64, v159
	s_add_i32 m0, s57, 0x2000
	s_add_u32 s70, s20, 0x20000
	global_load_lds_dwordx4 v64, s[20:21]
	s_addc_u32 s71, s21, 0
	v_mov_b32_e32 v64, v157
	s_add_i32 s57, s62, s25
	s_mov_b32 m0, s57
	s_nop 0
	global_load_lds_dwordx4 v64, s[70:71]
	v_mov_b32_e32 v64, v159
	s_add_i32 m0, s57, 0x2000
	s_nop 0
	global_load_lds_dwordx4 v64, s[70:71]
	v_mov_b32_e32 v64, v156
	s_mov_b32 m0, s26
	s_nop 0
	global_load_lds_dwordx4 v64, s[8:9]
	v_mov_b32_e32 v64, v158
	s_mov_b32 m0, s27
	s_nop 0
	global_load_lds_dwordx4 v64, s[8:9]
	s_cmp_eq_u32 s99, 0
	s_cbranch_scc1 .Lrw_q2_n
	s_waitcnt vmcnt(24)
	s_branch .Lrw_q2_d

.Lrw_q2_d:
	s_mov_b32 s99, 0
	s_waitcnt lgkmcnt(0)
	s_barrier
	s_setprio 1
	s_waitcnt lgkmcnt(0)
	v_mfma_f32_16x16x128_f8f6f4 v[60:63], v[130:137], v[66:73], v[60:63]
	v_mfma_f32_16x16x128_f8f6f4 v[56:59], v[138:145], v[66:73], v[56:59]
	v_mfma_f32_16x16x128_f8f6f4 v[188:191], v[130:137], v[74:81], v[44:47]
	v_mfma_f32_16x16x128_f8f6f4 v[192:195], v[138:145], v[74:81], v[40:43]
	v_mfma_f32_16x16x128_f8f6f4 v[196:199], v[130:137], v[82:89], v[28:31]
	v_mfma_f32_16x16x128_f8f6f4 v[200:203], v[138:145], v[82:89], v[24:27]
	v_mfma_f32_16x16x128_f8f6f4 v[230:233], v[130:137], v[90:97], v[12:15]
	v_mfma_f32_16x16x128_f8f6f4 v[234:237], v[138:145], v[90:97], v[8:11]
	s_setprio 0
	s_setprio 1
	v_mfma_f32_16x16x128_f8f6f4 v[52:55], v[146:153], v[66:73], v[52:55]
	v_mfma_f32_16x16x128_f8f6f4 v[48:51], v[164:171], v[66:73], v[48:51]
	v_mfma_f32_16x16x128_f8f6f4 v[238:241], v[146:153], v[74:81], v[36:39]
	v_mfma_f32_16x16x128_f8f6f4 v[242:245], v[164:171], v[74:81], v[32:35]
	v_mfma_f32_16x16x128_f8f6f4 v[246:249], v[146:153], v[82:89], v[20:23]
	v_mfma_f32_16x16x128_f8f6f4 v[250:253], v[164:171], v[82:89], v[16:19]
	v_mfma_f32_16x16x128_f8f6f4 v[224:227], v[146:153], v[90:97], v[4:7]
	v_mfma_f32_16x16x128_f8f6f4 v[220:223], v[164:171], v[90:97], v[0:3]
	s_setprio 0
	s_barrier
	s_add_i32 s57, 0, 0x18000
	v_add_u32_e32 v8, s57, v162
	s_add_i32 s62, 0, 0x1c000
	s_nop 1
	ds_read_b128 v[0:3], v8
	ds_read_b128 v[4:7], v8 offset:1024
	ds_read_b128 v[16:19], v8 offset:2048
	ds_read_b128 v[20:23], v8 offset:3072
	v_add_u32_e32 v8, s62, v162
	ds_read_b128 v[130:133], v8
	ds_read_b128 v[134:137], v8 offset:1024
	ds_read_b128 v[138:141], v8 offset:2048
	ds_read_b128 v[142:145], v8 offset:3072
	s_add_u32 s70, s8, 0x20000
	v_mov_b32_e32 v64, v156
	s_mov_b32 m0, s28
	ds_read_b128 v[8:11], v163 offset:32768
	ds_read_b128 v[12:15], v163 offset:33792
	ds_read_b128 v[24:27], v163 offset:34816
	ds_read_b128 v[28:31], v163 offset:35840
	ds_read_b128 v[32:35], v163 offset:36864
	ds_read_b128 v[36:39], v163 offset:37888
	ds_read_b128 v[40:43], v163 offset:38912
	ds_read_b128 v[44:47], v163 offset:39936
	s_addc_u32 s71, s9, 0
	s_nop 0
	global_load_lds_dwordx4 v64, s[70:71]
	v_mov_b32_e32 v64, v158
	s_mov_b32 m0, s29
	s_nop 0
	global_load_lds_dwordx4 v64, s[70:71]
	s_waitcnt vmcnt(8)
	s_waitcnt lgkmcnt(0)
	s_barrier
	s_setprio 1
	s_waitcnt lgkmcnt(0)
	v_mfma_f32_16x16x128_f8f6f4 v[126:129], v[0:7], v[8:15], v[126:129]
	v_mfma_f32_16x16x128_f8f6f4 v[122:125], v[16:23], v[8:15], v[122:125]
	v_mfma_f32_16x16x128_f8f6f4 v[110:113], v[0:7], v[24:31], v[110:113]
	v_mfma_f32_16x16x128_f8f6f4 v[106:109], v[16:23], v[24:31], v[106:109]
	v_mfma_f32_16x16x128_f8f6f4 v[94:97], v[0:7], v[32:39], v[204:207]
	v_mfma_f32_16x16x128_f8f6f4 v[90:93], v[16:23], v[32:39], v[208:211]
	v_mfma_f32_16x16x128_f8f6f4 v[78:81], v[0:7], v[40:47], v[212:215]
	v_mfma_f32_16x16x128_f8f6f4 v[74:77], v[16:23], v[40:47], v[216:219]
	s_setprio 0
	s_setprio 1
	v_mfma_f32_16x16x128_f8f6f4 v[118:121], v[130:137], v[8:15], v[118:121]
	v_mfma_f32_16x16x128_f8f6f4 v[114:117], v[138:145], v[8:15], v[114:117]
	v_mfma_f32_16x16x128_f8f6f4 v[102:105], v[130:137], v[24:31], v[102:105]
	v_mfma_f32_16x16x128_f8f6f4 v[98:101], v[138:145], v[24:31], v[98:101]
	v_mfma_f32_16x16x128_f8f6f4 v[86:89], v[130:137], v[32:39], v[172:175]
	v_mfma_f32_16x16x128_f8f6f4 v[82:85], v[138:145], v[32:39], v[176:179]
	v_mfma_f32_16x16x128_f8f6f4 v[70:73], v[130:137], v[40:47], v[180:183]
	v_mfma_f32_16x16x128_f8f6f4 v[66:69], v[138:145], v[40:47], v[184:187]
	s_setprio 0
	s_barrier
	v_mov_b32_e32 v64, v157
	ds_read_b128 v[32:35], v163 offset:49152
	ds_read_b128 v[36:39], v163 offset:50176
	ds_read_b128 v[146:149], v163 offset:51200
	ds_read_b128 v[150:153], v163 offset:52224
	ds_read_b128 v[164:167], v163 offset:53248
	ds_read_b128 v[168:171], v163 offset:54272
	ds_read_b128 v[172:175], v163 offset:55296
	ds_read_b128 v[176:179], v163 offset:56320
	s_add_i32 s57, s57, s25
	v_lshl_add_u64 v[8:9], s[20:21], 0, v[64:65]
	v_lshl_add_u64 v[8:9], v[8:9], 0, s[80:81]
	s_mov_b32 m0, s57
	v_mov_b32_e32 v64, v159
	global_load_lds_dwordx4 v[8:9], off
	s_add_i32 m0, s57, 0x2000
	v_lshl_add_u64 v[8:9], s[20:21], 0, v[64:65]
	v_lshl_add_u64 v[8:9], v[8:9], 0, s[80:81]
	s_add_u32 s20, s20, 0x20080
	global_load_lds_dwordx4 v[8:9], off
	s_addc_u32 s21, s21, 0
	v_mov_b32_e32 v8, v157
	s_add_i32 s57, s62, s25
	s_mov_b32 m0, s57
	v_mov_b32_e32 v64, v156
	global_load_lds_dwordx4 v8, s[20:21]
	v_mov_b32_e32 v8, v159
	s_add_i32 m0, s57, 0x2000
	s_nop 0
	global_load_lds_dwordx4 v8, s[20:21]
	s_mov_b32 m0, s31
	v_lshl_add_u64 v[8:9], s[8:9], 0, v[64:65]
	v_lshl_add_u64 v[8:9], v[8:9], 0, s[80:81]
	v_mov_b32_e32 v64, v158
	global_load_lds_dwordx4 v[8:9], off
	s_mov_b32 m0, s34
	v_lshl_add_u64 v[8:9], s[8:9], 0, v[64:65]
	v_lshl_add_u64 v[8:9], v[8:9], 0, s[80:81]
	global_load_lds_dwordx4 v[8:9], off
	s_waitcnt vmcnt(8)
	s_waitcnt lgkmcnt(0)
	s_barrier
	s_setprio 1
	s_waitcnt lgkmcnt(0)
	v_mfma_f32_16x16x128_f8f6f4 v[60:63], v[0:7], v[32:39], v[60:63]
	v_mfma_f32_16x16x128_f8f6f4 v[56:59], v[16:23], v[32:39], v[56:59]
	v_mfma_f32_16x16x128_f8f6f4 v[44:47], v[0:7], v[146:153], v[188:191]
	v_mfma_f32_16x16x128_f8f6f4 v[40:43], v[16:23], v[146:153], v[192:195]
	v_mfma_f32_16x16x128_f8f6f4 v[28:31], v[0:7], v[164:171], v[196:199]
	v_mfma_f32_16x16x128_f8f6f4 v[24:27], v[16:23], v[164:171], v[200:203]
	v_mfma_f32_16x16x128_f8f6f4 v[12:15], v[0:7], v[172:179], v[230:233]
	v_mfma_f32_16x16x128_f8f6f4 v[8:11], v[16:23], v[172:179], v[234:237]
	s_setprio 0
	s_setprio 1
	v_mfma_f32_16x16x128_f8f6f4 v[52:55], v[130:137], v[32:39], v[52:55]
	v_mfma_f32_16x16x128_f8f6f4 v[48:51], v[138:145], v[32:39], v[48:51]
	v_mfma_f32_16x16x128_f8f6f4 v[36:39], v[130:137], v[146:153], v[238:241]
	v_mfma_f32_16x16x128_f8f6f4 v[32:35], v[138:145], v[146:153], v[242:245]
	v_mfma_f32_16x16x128_f8f6f4 v[20:23], v[130:137], v[164:171], v[246:249]
	v_mfma_f32_16x16x128_f8f6f4 v[16:19], v[138:145], v[164:171], v[250:253]
	v_mfma_f32_16x16x128_f8f6f4 v[4:7], v[130:137], v[172:179], v[224:227]
	v_mfma_f32_16x16x128_f8f6f4 v[0:3], v[138:145], v[172:179], v[220:223]
	s_setprio 0
	s_barrier
	s_add_i32 s56, s56, 2
	s_add_u32 s6, s6, 0x100
	s_addc_u32 s7, s7, 0
	s_add_u32 s39, s39, 0x100
	s_addc_u32 s49, s49, 0
	s_cmp_gt_u32 s56, 5
	s_cbranch_scc0 .LBB0_261
	s_and_b64 vcc, exec, s[14:15]
	s_cbranch_vccz .LBB0_264
	s_barrier

.LBB0_345:
	v_pk_mul_f32 v[4:5], v[150:151], v[4:5]
	s_waitcnt lgkmcnt(0)
	v_pk_mul_f32 v[8:9], v[34:35], v[2:3]
	v_pk_mul_f32 v[2:3], v[150:151], v[0:1]
	v_cvt_pk_bf16_f32 v0, v4, v5
	v_or_b32_e32 v4, 0x4000, v32
	v_ashrrev_i32_e32 v5, 31, v4
	v_lshlrev_b64 v[4:5], 7, v[4:5]
	v_lshl_add_u64 v[4:5], s[20:21], 0, v[4:5]
	v_lshl_add_u64 v[4:5], v[148:149], 1, v[4:5]
	v_pk_mul_f32 v[6:7], v[34:35], v[6:7]
	s_nop 0
	v_cvt_pk_bf16_f32 v1, v6, v7
	v_cvt_pk_bf16_f32 v2, v2, v3
	v_cvt_pk_bf16_f32 v3, v8, v9
	global_store_dwordx4 v[4:5], v[0:3], off nt sc1
	s_mov_b32 s99, 1
	s_cmp_eq_u32 s38, 11
	s_mov_b64 s[6:7], -1
	s_cbranch_scc1 .LBB0_259
	s_andn2_b64 vcc, exec, s[12:13]
	s_cbranch_vccnz .LBB0_258
	s_barrier
	s_branch .LBB0_258

.LBB0_349:
	s_mov_b32 s99, 0
	v_mbcnt_lo_u32_b32 v0, -1, 0
	v_mbcnt_hi_u32_b32 v0, -1, v0
	v_mov_b32_e32 v8, 1
	v_add_u32_e32 v1, s24, v0
	v_ashrrev_i32_e32 v3, 31, v1
	v_lshrrev_b32_e32 v3, 26, v3
	v_readfirstlane_b32 s10, v1
	v_lshlrev_b32_e32 v2, 4, v1
	v_add_u32_e32 v3, v1, v3
	v_bfe_i32 v1, v1, 27, 1
	v_lshrrev_b32_e32 v1, 22, v1
	v_add_u32_e32 v1, v2, v1
	v_and_b32_e32 v1, 0xfffffc00, v1
	v_sub_u32_e32 v1, v2, v1
	v_lshrrev_b32_e32 v4, 4, v1
	v_bitop3_b32 v1, v4, v1, 32 bitop3:0x6c
	v_ashrrev_i32_e32 v5, 31, v1
	v_ashrrev_i32_e32 v3, 6, v3
	v_lshrrev_b32_e32 v5, 26, v5
	v_lshlrev_b32_e32 v4, 3, v3
	v_add_u32_e32 v5, v1, v5
	v_and_b32_e32 v4, -16, v4
	v_ashrrev_i32_e32 v6, 6, v5
	v_and_b32_e32 v5, 0xc0, v5
	v_add_u32_e32 v4, v6, v4
	v_sub_u32_e32 v1, v1, v5
	v_lshlrev_b32_e32 v3, 5, v3
	v_ashrrev_i16_sdwa v1, v8, sext(v1) dst_sel:DWORD dst_unused:UNUSED_PAD src0_sel:DWORD src1_sel:BYTE_0
	v_lshlrev_b32_e32 v5, 1, v4
	v_lshrrev_b32_e32 v7, 2, v4
	v_and_b32_e32 v6, 3, v6
	s_mov_b32 s11, 0x1fffe0
	v_and_b32_e32 v3, 32, v3
	v_bfe_i32 v1, v1, 0, 16
	v_and_b32_e32 v5, 24, v5
	v_and_b32_e32 v7, 4, v7
	v_and_or_b32 v6, v4, s11, v6
	v_or3_b32 v5, v6, v7, v5
	v_add_lshl_u32 v1, v3, v1, 1
	v_lshl_add_u32 v134, v4, 11, v1
	v_lshl_add_u32 v135, v5, 11, v1
	v_add_u32_e32 v1, 0x2000, v2
	v_ashrrev_i32_e32 v2, 31, v1
	v_lshrrev_b32_e32 v2, 22, v2
	v_add_u32_e32 v2, v1, v2
	v_ashrrev_i32_e32 v2, 10, v2
	v_mul_i32_i24_e32 v3, 0x400, v2
	v_sub_u32_e32 v1, v1, v3
	v_lshrrev_b32_e32 v3, 4, v1
	v_bitop3_b32 v1, v3, v1, 32 bitop3:0x6c
	v_ashrrev_i32_e32 v4, 31, v1
	s_mul_i32 s66, s45, 0x2c0000
	v_lshrrev_b32_e32 v4, 26, v4
	s_lshl_b64 s[6:7], s[66:67], 1
	v_readlane_b32 s8, v254, 14
	v_lshlrev_b32_e32 v3, 3, v2
	v_add_u32_e32 v4, v1, v4
	v_readlane_b32 s9, v254, 15
	s_add_u32 s6, s8, s6
	v_and_b32_e32 v3, -16, v3
	v_ashrrev_i32_e32 v5, 6, v4
	v_and_b32_e32 v4, 0xc0, v4
	s_addc_u32 s7, s9, s7
	v_add_u32_e32 v3, v5, v3
	v_sub_u32_e32 v1, v1, v4
	s_add_u32 s8, s6, 0x40000
	v_lshlrev_b32_e32 v2, 5, v2
	v_ashrrev_i16_sdwa v1, v8, sext(v1) dst_sel:DWORD dst_unused:UNUSED_PAD src0_sel:DWORD src1_sel:BYTE_0
	v_lshlrev_b32_e32 v4, 1, v3
	v_lshrrev_b32_e32 v6, 2, v3
	v_and_b32_e32 v5, 3, v5
	s_addc_u32 s9, s7, 0
	v_and_b32_e32 v2, 32, v2
	v_bfe_i32 v1, v1, 0, 16
	v_and_b32_e32 v4, 24, v4
	v_and_b32_e32 v6, 4, v6
	v_and_or_b32 v5, v3, s11, v5
	s_ashr_i32 s11, s10, 6
	v_or3_b32 v4, v5, v6, v4
	v_add_lshl_u32 v1, v2, v1, 1
	s_lshl_b32 s20, s11, 10
	v_lshl_add_u32 v136, v3, 11, v1
	v_lshl_add_u32 v137, v4, 11, v1
	s_add_i32 s21, s20, 0
	v_mov_b32_e32 v1, v135
	s_add_i32 m0, s21, 0x10000
	s_add_i32 s22, s21, 0x2000
	global_load_lds_dwordx4 v1, s[6:7]
	v_mov_b32_e32 v1, v137
	s_add_i32 m0, s21, 0x12000
	s_add_i32 s23, s21, 0x4000
	global_load_lds_dwordx4 v1, s[6:7]
	v_mov_b32_e32 v1, v135
	s_add_i32 m0, s21, 0x14000
	s_add_i32 s24, s21, 0x6000
	global_load_lds_dwordx4 v1, s[8:9]
	v_mov_b32_e32 v1, v137
	s_add_i32 m0, s21, 0x16000
	s_ashr_i32 s12, s10, 8
	global_load_lds_dwordx4 v1, s[8:9]
	v_mov_b32_e32 v1, v134
	s_mov_b32 m0, s21
	v_readlane_b32 s8, v254, 28
	global_load_lds_dwordx4 v1, s[72:73]
	v_mov_b32_e32 v1, v136
	s_mov_b32 m0, s22
	v_readlane_b32 s9, v254, 29
	global_load_lds_dwordx4 v1, s[72:73]
	v_mov_b32_e32 v1, v134
	s_mov_b32 m0, s23
	s_cmp_eq_u32 s12, 1
	s_nop 0
	global_load_lds_dwordx4 v1, s[8:9]
	v_mov_b32_e32 v1, v136
	s_mov_b32 m0, s24
	s_nop 0
	global_load_lds_dwordx4 v1, s[8:9]
	s_cselect_b64 s[8:9], -1, 0
	s_cmp_lg_u32 s12, 1
	s_cbranch_scc1 .LBB0_351
	s_barrier

.LBB0_355:
	s_add_u32 s16, s14, 0xfffc0080
	s_addc_u32 s17, s15, -1
	s_add_i32 s39, 0, 0x10000
	s_cmp_eq_u32 s38, 12
	s_cselect_b32 s17, s73, s17
	s_cselect_b32 s16, s72, s16
	v_add_u32_e32 v64, s39, v140
	s_cselect_b32 s19, s34, s37
	s_cselect_b32 s18, s35, s36
	s_add_i32 s49, 0, 0x14000
	ds_read_b128 v[130:133], v64
	ds_read_b128 v[142:145], v64 offset:1024
	ds_read_b128 v[146:149], v64 offset:2048
	ds_read_b128 v[150:153], v64 offset:3072
	v_add_u32_e32 v64, s49, v140
	ds_read_b128 v[154:157], v64
	ds_read_b128 v[158:161], v64 offset:1024
	ds_read_b128 v[162:165], v64 offset:2048
	ds_read_b128 v[166:169], v64 offset:3072
	v_mov_b32_e32 v64, v134
	ds_read_b128 v[170:173], v141
	ds_read_b128 v[174:177], v141 offset:1024
	ds_read_b128 v[178:181], v141 offset:2048
	ds_read_b128 v[182:185], v141 offset:3072
	ds_read_b128 v[186:189], v141 offset:4096
	ds_read_b128 v[190:193], v141 offset:5120
	ds_read_b128 v[194:197], v141 offset:6144
	ds_read_b128 v[198:201], v141 offset:7168
	s_add_i32 m0, s21, 0xc000
	s_nop 0
	global_load_lds_dwordx4 v64, s[14:15]
	v_mov_b32_e32 v64, v136
	s_add_i32 m0, s21, 0xe000
	s_nop 0
	global_load_lds_dwordx4 v64, s[14:15]
	s_cmp_eq_u32 s99, 0
	s_cbranch_scc1 .Lrw_i1_n
	s_cmp_eq_u32 s99, 1
	s_cbranch_scc0 .Lrw_i1_0
	s_waitcnt vmcnt(16)
	s_branch .Lrw_i1_d
.Lrw_i1_0:
	s_waitcnt vmcnt(24)
	s_branch .Lrw_i1_d

.Lrw_i1_d:
	s_waitcnt lgkmcnt(0)
	s_barrier
	s_setprio 1
	s_waitcnt lgkmcnt(0)
	v_mfma_f32_16x16x32_bf16 v[126:129], v[130:133], v[170:173], v[126:129]
	v_mfma_f32_16x16x32_bf16 v[122:125], v[146:149], v[170:173], v[122:125]
	v_mfma_f32_16x16x32_bf16 v[118:121], v[130:133], v[178:181], v[118:121]
	v_mfma_f32_16x16x32_bf16 v[110:113], v[146:149], v[178:181], v[110:113]
	v_mfma_f32_16x16x32_bf16 v[102:105], v[130:133], v[186:189], v[102:105]
	v_mfma_f32_16x16x32_bf16 v[94:97], v[146:149], v[186:189], v[94:97]
	v_mfma_f32_16x16x32_bf16 v[86:89], v[130:133], v[194:197], v[86:89]
	v_mfma_f32_16x16x32_bf16 v[78:81], v[146:149], v[194:197], v[78:81]
	v_mfma_f32_16x16x32_bf16 v[126:129], v[142:145], v[174:177], v[126:129]
	v_mfma_f32_16x16x32_bf16 v[122:125], v[150:153], v[174:177], v[122:125]
	v_mfma_f32_16x16x32_bf16 v[118:121], v[142:145], v[182:185], v[118:121]
	v_mfma_f32_16x16x32_bf16 v[110:113], v[150:153], v[182:185], v[110:113]
	v_mfma_f32_16x16x32_bf16 v[102:105], v[142:145], v[190:193], v[102:105]
	v_mfma_f32_16x16x32_bf16 v[94:97], v[150:153], v[190:193], v[94:97]
	v_mfma_f32_16x16x32_bf16 v[86:89], v[142:145], v[198:201], v[86:89]
	v_mfma_f32_16x16x32_bf16 v[78:81], v[150:153], v[198:201], v[78:81]
	s_setprio 0
	s_setprio 1
	v_mfma_f32_16x16x32_bf16 v[114:117], v[154:157], v[170:173], v[114:117]
	v_mfma_f32_16x16x32_bf16 v[106:109], v[162:165], v[170:173], v[106:109]
	v_mfma_f32_16x16x32_bf16 v[98:101], v[154:157], v[178:181], v[98:101]
	v_mfma_f32_16x16x32_bf16 v[90:93], v[162:165], v[178:181], v[90:93]
	v_mfma_f32_16x16x32_bf16 v[82:85], v[154:157], v[186:189], v[82:85]
	v_mfma_f32_16x16x32_bf16 v[74:77], v[162:165], v[186:189], v[74:77]
	v_mfma_f32_16x16x32_bf16 v[70:73], v[154:157], v[194:197], v[70:73]
	v_mfma_f32_16x16x32_bf16 v[66:69], v[162:165], v[194:197], v[66:69]
	v_mfma_f32_16x16x32_bf16 v[114:117], v[158:161], v[174:177], v[114:117]
	v_mfma_f32_16x16x32_bf16 v[106:109], v[166:169], v[174:177], v[106:109]
	v_mfma_f32_16x16x32_bf16 v[98:101], v[158:161], v[182:185], v[98:101]
	v_mfma_f32_16x16x32_bf16 v[90:93], v[166:169], v[182:185], v[90:93]
	v_mfma_f32_16x16x32_bf16 v[82:85], v[158:161], v[190:193], v[82:85]
	v_mfma_f32_16x16x32_bf16 v[74:77], v[166:169], v[190:193], v[74:77]
	v_mfma_f32_16x16x32_bf16 v[70:73], v[158:161], v[198:201], v[70:73]
	v_mfma_f32_16x16x32_bf16 v[66:69], v[166:169], v[198:201], v[66:69]
	s_setprio 0
	s_barrier
	v_mov_b32_e32 v64, v135
	s_add_i32 s39, s39, s20
	ds_read_b128 v[170:173], v141 offset:16384
	ds_read_b128 v[174:177], v141 offset:17408
	ds_read_b128 v[178:181], v141 offset:18432
	ds_read_b128 v[182:185], v141 offset:19456
	ds_read_b128 v[186:189], v141 offset:20480
	ds_read_b128 v[190:193], v141 offset:21504
	ds_read_b128 v[194:197], v141 offset:22528
	ds_read_b128 v[198:201], v141 offset:23552
	s_mov_b32 m0, s39
	s_nop 0
	global_load_lds_dwordx4 v64, s[18:19]
	v_mov_b32_e32 v64, v137
	s_add_i32 m0, s39, 0x2000
	s_add_u32 s56, s18, 0x40000
	global_load_lds_dwordx4 v64, s[18:19]
	s_addc_u32 s57, s19, 0
	v_mov_b32_e32 v64, v135
	s_add_i32 s39, s49, s20
	s_mov_b32 m0, s39
	s_nop 0
	global_load_lds_dwordx4 v64, s[56:57]
	v_mov_b32_e32 v64, v137
	s_add_i32 m0, s39, 0x2000
	s_nop 0
	global_load_lds_dwordx4 v64, s[56:57]
	v_mov_b32_e32 v64, v134
	s_mov_b32 m0, s21
	s_nop 0
	global_load_lds_dwordx4 v64, s[16:17]
	v_mov_b32_e32 v64, v136
	s_mov_b32 m0, s22
	s_nop 0
	global_load_lds_dwordx4 v64, s[16:17]
	s_cmp_eq_u32 s99, 0
	s_cbranch_scc1 .Lrw_i2_n
	s_cmp_eq_u32 s99, 1
	s_cbranch_scc0 .Lrw_i2_0
	s_waitcnt vmcnt(16)
	s_branch .Lrw_i2_d

.Lrw_i2_d:
	s_mov_b32 s99, 0
	s_waitcnt lgkmcnt(0)
	s_barrier
	s_setprio 1
	s_waitcnt lgkmcnt(0)
	v_mfma_f32_16x16x32_bf16 v[60:63], v[130:133], v[170:173], v[60:63]
	v_mfma_f32_16x16x32_bf16 v[56:59], v[146:149], v[170:173], v[56:59]
	v_mfma_f32_16x16x32_bf16 v[52:55], v[130:133], v[178:181], v[52:55]
	v_mfma_f32_16x16x32_bf16 v[44:47], v[146:149], v[178:181], v[44:47]
	v_mfma_f32_16x16x32_bf16 v[36:39], v[130:133], v[186:189], v[36:39]
	v_mfma_f32_16x16x32_bf16 v[28:31], v[146:149], v[186:189], v[28:31]
	v_mfma_f32_16x16x32_bf16 v[20:23], v[130:133], v[194:197], v[20:23]
	v_mfma_f32_16x16x32_bf16 v[12:15], v[146:149], v[194:197], v[12:15]
	v_mfma_f32_16x16x32_bf16 v[60:63], v[142:145], v[174:177], v[60:63]
	v_mfma_f32_16x16x32_bf16 v[56:59], v[150:153], v[174:177], v[56:59]
	v_mfma_f32_16x16x32_bf16 v[52:55], v[142:145], v[182:185], v[52:55]
	v_mfma_f32_16x16x32_bf16 v[44:47], v[150:153], v[182:185], v[44:47]
	v_mfma_f32_16x16x32_bf16 v[36:39], v[142:145], v[190:193], v[36:39]
	v_mfma_f32_16x16x32_bf16 v[28:31], v[150:153], v[190:193], v[28:31]
	v_mfma_f32_16x16x32_bf16 v[20:23], v[142:145], v[198:201], v[20:23]
	v_mfma_f32_16x16x32_bf16 v[12:15], v[150:153], v[198:201], v[12:15]
	s_setprio 0
	s_setprio 1
	v_mfma_f32_16x16x32_bf16 v[48:51], v[154:157], v[170:173], v[48:51]
	v_mfma_f32_16x16x32_bf16 v[40:43], v[162:165], v[170:173], v[40:43]
	v_mfma_f32_16x16x32_bf16 v[32:35], v[154:157], v[178:181], v[32:35]
	v_mfma_f32_16x16x32_bf16 v[24:27], v[162:165], v[178:181], v[24:27]
	v_mfma_f32_16x16x32_bf16 v[16:19], v[154:157], v[186:189], v[16:19]
	v_mfma_f32_16x16x32_bf16 v[8:11], v[162:165], v[186:189], v[8:11]
	v_mfma_f32_16x16x32_bf16 v[4:7], v[154:157], v[194:197], v[4:7]
	v_mfma_f32_16x16x32_bf16 v[0:3], v[162:165], v[194:197], v[0:3]
	v_mfma_f32_16x16x32_bf16 v[48:51], v[158:161], v[174:177], v[48:51]
	v_mfma_f32_16x16x32_bf16 v[40:43], v[166:169], v[174:177], v[40:43]
	v_mfma_f32_16x16x32_bf16 v[32:35], v[158:161], v[182:185], v[32:35]
	v_mfma_f32_16x16x32_bf16 v[24:27], v[166:169], v[182:185], v[24:27]
	v_mfma_f32_16x16x32_bf16 v[16:19], v[158:161], v[190:193], v[16:19]
	v_mfma_f32_16x16x32_bf16 v[8:11], v[166:169], v[190:193], v[8:11]
	v_mfma_f32_16x16x32_bf16 v[4:7], v[158:161], v[198:201], v[4:7]
	v_mfma_f32_16x16x32_bf16 v[0:3], v[166:169], v[198:201], v[0:3]
	s_setprio 0
	s_barrier
	s_add_i32 s39, 0, 0x18000
	v_add_u32_e32 v64, s39, v140
	s_add_i32 s49, 0, 0x1c000
	ds_read_b128 v[130:133], v64
	ds_read_b128 v[142:145], v64 offset:1024
	ds_read_b128 v[146:149], v64 offset:2048
	ds_read_b128 v[150:153], v64 offset:3072
	v_add_u32_e32 v64, s49, v140
	ds_read_b128 v[154:157], v64
	ds_read_b128 v[158:161], v64 offset:1024
	ds_read_b128 v[162:165], v64 offset:2048
	ds_read_b128 v[166:169], v64 offset:3072
	s_add_u32 s56, s16, 0x40000
	v_mov_b32_e32 v64, v134
	s_mov_b32 m0, s23
	ds_read_b128 v[170:173], v141 offset:32768
	ds_read_b128 v[174:177], v141 offset:33792
	ds_read_b128 v[178:181], v141 offset:34816
	ds_read_b128 v[182:185], v141 offset:35840
	ds_read_b128 v[186:189], v141 offset:36864
	ds_read_b128 v[190:193], v141 offset:37888
	ds_read_b128 v[194:197], v141 offset:38912
	ds_read_b128 v[198:201], v141 offset:39936
	s_addc_u32 s57, s17, 0
	s_nop 0
	global_load_lds_dwordx4 v64, s[56:57]
	v_mov_b32_e32 v64, v136
	s_mov_b32 m0, s24
	s_nop 0
	global_load_lds_dwordx4 v64, s[56:57]
	s_waitcnt vmcnt(8)
	s_waitcnt lgkmcnt(0)
	s_barrier
	s_setprio 1
	s_waitcnt lgkmcnt(0)
	v_mfma_f32_16x16x32_bf16 v[126:129], v[130:133], v[170:173], v[126:129]
	v_mfma_f32_16x16x32_bf16 v[122:125], v[146:149], v[170:173], v[122:125]
	v_mfma_f32_16x16x32_bf16 v[118:121], v[130:133], v[178:181], v[118:121]
	v_mfma_f32_16x16x32_bf16 v[110:113], v[146:149], v[178:181], v[110:113]
	v_mfma_f32_16x16x32_bf16 v[102:105], v[130:133], v[186:189], v[102:105]
	v_mfma_f32_16x16x32_bf16 v[94:97], v[146:149], v[186:189], v[94:97]
	v_mfma_f32_16x16x32_bf16 v[86:89], v[130:133], v[194:197], v[86:89]
	v_mfma_f32_16x16x32_bf16 v[78:81], v[146:149], v[194:197], v[78:81]
	v_mfma_f32_16x16x32_bf16 v[126:129], v[142:145], v[174:177], v[126:129]
	v_mfma_f32_16x16x32_bf16 v[122:125], v[150:153], v[174:177], v[122:125]
	v_mfma_f32_16x16x32_bf16 v[118:121], v[142:145], v[182:185], v[118:121]
	v_mfma_f32_16x16x32_bf16 v[110:113], v[150:153], v[182:185], v[110:113]
	v_mfma_f32_16x16x32_bf16 v[102:105], v[142:145], v[190:193], v[102:105]
	v_mfma_f32_16x16x32_bf16 v[94:97], v[150:153], v[190:193], v[94:97]
	v_mfma_f32_16x16x32_bf16 v[86:89], v[142:145], v[198:201], v[86:89]
	v_mfma_f32_16x16x32_bf16 v[78:81], v[150:153], v[198:201], v[78:81]
	s_setprio 0
	s_setprio 1
	v_mfma_f32_16x16x32_bf16 v[114:117], v[154:157], v[170:173], v[114:117]
	v_mfma_f32_16x16x32_bf16 v[106:109], v[162:165], v[170:173], v[106:109]
	v_mfma_f32_16x16x32_bf16 v[98:101], v[154:157], v[178:181], v[98:101]
	v_mfma_f32_16x16x32_bf16 v[90:93], v[162:165], v[178:181], v[90:93]
	v_mfma_f32_16x16x32_bf16 v[82:85], v[154:157], v[186:189], v[82:85]
	v_mfma_f32_16x16x32_bf16 v[74:77], v[162:165], v[186:189], v[74:77]
	v_mfma_f32_16x16x32_bf16 v[70:73], v[154:157], v[194:197], v[70:73]
	v_mfma_f32_16x16x32_bf16 v[66:69], v[162:165], v[194:197], v[66:69]
	v_mfma_f32_16x16x32_bf16 v[114:117], v[158:161], v[174:177], v[114:117]
	v_mfma_f32_16x16x32_bf16 v[106:109], v[166:169], v[174:177], v[106:109]
	v_mfma_f32_16x16x32_bf16 v[98:101], v[158:161], v[182:185], v[98:101]
	v_mfma_f32_16x16x32_bf16 v[90:93], v[166:169], v[182:185], v[90:93]
	v_mfma_f32_16x16x32_bf16 v[82:85], v[158:161], v[190:193], v[82:85]
	v_mfma_f32_16x16x32_bf16 v[74:77], v[166:169], v[190:193], v[74:77]
	v_mfma_f32_16x16x32_bf16 v[70:73], v[158:161], v[198:201], v[70:73]
	v_mfma_f32_16x16x32_bf16 v[66:69], v[166:169], v[198:201], v[66:69]
	s_setprio 0
	s_barrier
	v_mov_b32_e32 v64, v135
	ds_read_b128 v[170:173], v141 offset:49152
	ds_read_b128 v[174:177], v141 offset:50176
	ds_read_b128 v[178:181], v141 offset:51200
	ds_read_b128 v[182:185], v141 offset:52224
	ds_read_b128 v[186:189], v141 offset:53248
	ds_read_b128 v[190:193], v141 offset:54272
	ds_read_b128 v[194:197], v141 offset:55296
	ds_read_b128 v[198:201], v141 offset:56320
	s_add_i32 s39, s39, s20
	v_lshl_add_u64 v[202:203], s[18:19], 0, v[64:65]
	v_lshl_add_u64 v[202:203], v[202:203], 0, s[80:81]
	s_mov_b32 m0, s39
	v_mov_b32_e32 v64, v137
	global_load_lds_dwordx4 v[202:203], off
	s_add_i32 m0, s39, 0x2000
	s_nop 0
	v_lshl_add_u64 v[202:203], s[18:19], 0, v[64:65]
	s_add_u32 s18, s18, 0x40080
	v_lshl_add_u64 v[202:203], v[202:203], 0, s[80:81]
	s_addc_u32 s19, s19, 0
	v_mov_b32_e32 v64, v135
	s_add_i32 s39, s49, s20
	global_load_lds_dwordx4 v[202:203], off
	s_mov_b32 m0, s39
	s_nop 0
	global_load_lds_dwordx4 v64, s[18:19]
	v_mov_b32_e32 v64, v137
	s_add_i32 m0, s39, 0x2000
	s_nop 0
	global_load_lds_dwordx4 v64, s[18:19]
	v_mov_b32_e32 v64, v134
	s_mov_b32 m0, s27
	v_lshl_add_u64 v[202:203], s[16:17], 0, v[64:65]
	v_lshl_add_u64 v[202:203], v[202:203], 0, s[80:81]
	v_mov_b32_e32 v64, v136
	global_load_lds_dwordx4 v[202:203], off
	s_mov_b32 m0, s28
	v_lshl_add_u64 v[202:203], s[16:17], 0, v[64:65]
	v_lshl_add_u64 v[202:203], v[202:203], 0, s[80:81]
	global_load_lds_dwordx4 v[202:203], off
	s_waitcnt vmcnt(8)
	s_waitcnt lgkmcnt(0)
	s_barrier
	s_setprio 1
	s_waitcnt lgkmcnt(0)
	v_mfma_f32_16x16x32_bf16 v[60:63], v[130:133], v[170:173], v[60:63]
	v_mfma_f32_16x16x32_bf16 v[56:59], v[146:149], v[170:173], v[56:59]
	v_mfma_f32_16x16x32_bf16 v[52:55], v[130:133], v[178:181], v[52:55]
	v_mfma_f32_16x16x32_bf16 v[44:47], v[146:149], v[178:181], v[44:47]
	v_mfma_f32_16x16x32_bf16 v[36:39], v[130:133], v[186:189], v[36:39]
	v_mfma_f32_16x16x32_bf16 v[28:31], v[146:149], v[186:189], v[28:31]
	v_mfma_f32_16x16x32_bf16 v[20:23], v[130:133], v[194:197], v[20:23]
	v_mfma_f32_16x16x32_bf16 v[12:15], v[146:149], v[194:197], v[12:15]
	v_mfma_f32_16x16x32_bf16 v[60:63], v[142:145], v[174:177], v[60:63]
	v_mfma_f32_16x16x32_bf16 v[56:59], v[150:153], v[174:177], v[56:59]
	v_mfma_f32_16x16x32_bf16 v[52:55], v[142:145], v[182:185], v[52:55]
	v_mfma_f32_16x16x32_bf16 v[44:47], v[150:153], v[182:185], v[44:47]
	v_mfma_f32_16x16x32_bf16 v[36:39], v[142:145], v[190:193], v[36:39]
	v_mfma_f32_16x16x32_bf16 v[28:31], v[150:153], v[190:193], v[28:31]
	v_mfma_f32_16x16x32_bf16 v[20:23], v[142:145], v[198:201], v[20:23]
	v_mfma_f32_16x16x32_bf16 v[12:15], v[150:153], v[198:201], v[12:15]
	s_setprio 0
	s_setprio 1
	v_mfma_f32_16x16x32_bf16 v[48:51], v[154:157], v[170:173], v[48:51]
	v_mfma_f32_16x16x32_bf16 v[40:43], v[162:165], v[170:173], v[40:43]
	v_mfma_f32_16x16x32_bf16 v[32:35], v[154:157], v[178:181], v[32:35]
	v_mfma_f32_16x16x32_bf16 v[24:27], v[162:165], v[178:181], v[24:27]
	v_mfma_f32_16x16x32_bf16 v[16:19], v[154:157], v[186:189], v[16:19]
	v_mfma_f32_16x16x32_bf16 v[8:11], v[162:165], v[186:189], v[8:11]
	v_mfma_f32_16x16x32_bf16 v[4:7], v[154:157], v[194:197], v[4:7]
	v_mfma_f32_16x16x32_bf16 v[0:3], v[162:165], v[194:197], v[0:3]
	v_mfma_f32_16x16x32_bf16 v[48:51], v[158:161], v[174:177], v[48:51]
	v_mfma_f32_16x16x32_bf16 v[40:43], v[166:169], v[174:177], v[40:43]
	v_mfma_f32_16x16x32_bf16 v[32:35], v[158:161], v[182:185], v[32:35]
	v_mfma_f32_16x16x32_bf16 v[24:27], v[166:169], v[182:185], v[24:27]
	v_mfma_f32_16x16x32_bf16 v[16:19], v[158:161], v[190:193], v[16:19]
	v_mfma_f32_16x16x32_bf16 v[8:11], v[166:169], v[190:193], v[8:11]
	v_mfma_f32_16x16x32_bf16 v[4:7], v[158:161], v[198:201], v[4:7]
	v_mfma_f32_16x16x32_bf16 v[0:3], v[166:169], v[198:201], v[0:3]
	s_setprio 0
	s_barrier
	s_add_i32 s38, s38, 2
	s_add_u32 s14, s14, 0x100
	s_addc_u32 s15, s15, 0
	s_add_u32 s36, s36, 0x100
	s_addc_u32 s37, s37, 0
	s_cmp_gt_u32 s38, 13
	s_cbranch_scc0 .LBB0_355
	s_and_b64 vcc, exec, s[10:11]
	s_cbranch_vccz .LBB0_358
	s_barrier

.LBB0_361:
	v_mul_f32_e32 v151, 0xbfb8aa3b, v107
	v_exp_f32_e32 v151, v151
	v_mul_f32_e32 v152, 0xbfb8aa3b, v116
	v_mul_f32_e32 v153, 0xbfb8aa3b, v108
	v_exp_f32_e32 v152, v152
	v_add_f32_e32 v151, 1.0, v151
	v_rcp_f32_e32 v151, v151
	v_exp_f32_e32 v153, v153
	v_mul_f32_e32 v130, 0xbfb8aa3b, v114
	v_mul_f32_e32 v131, 0xbfb8aa3b, v106
	v_mul_f32_e32 v150, 0xbfb8aa3b, v115
	v_mul_f32_e32 v154, v123, v151
	v_add_f32_e32 v151, 1.0, v152
	v_add_f32_e32 v152, 1.0, v153
	v_mul_f32_e32 v153, 0xbfb8aa3b, v117
	v_exp_f32_e32 v130, v130
	v_exp_f32_e32 v131, v131
	v_exp_f32_e32 v150, v150
	v_exp_f32_e32 v153, v153
	v_mul_f32_e32 v155, 0xbfb8aa3b, v109
	v_exp_f32_e32 v155, v155
	v_add_f32_e32 v130, 1.0, v130
	v_add_f32_e32 v131, 1.0, v131
	v_add_f32_e32 v150, 1.0, v150
	v_add_f32_e32 v153, 1.0, v153
	v_rcp_f32_e32 v130, v130
	v_rcp_f32_e32 v131, v131
	v_rcp_f32_e32 v150, v150
	v_rcp_f32_e32 v151, v151
	v_rcp_f32_e32 v152, v152
	v_rcp_f32_e32 v153, v153
	v_add_f32_e32 v155, 1.0, v155
	s_lshl_b32 s14, s31, 7
	v_rcp_f32_e32 v155, v155
	s_add_i32 s14, s29, s14
	v_add_u32_e32 v132, s14, v149
	v_mul_f32_e32 v130, v126, v130
	v_mul_f32_e32 v131, v122, v131
	v_mul_f32_e32 v150, v127, v150
	v_mul_f32_e32 v151, v128, v151
	v_mul_f32_e32 v156, v124, v152
	v_mul_f32_e32 v152, v129, v153
	v_ashrrev_i32_e32 v133, 31, v132
	v_cvt_pk_bf16_f32 v150, v130, v150
	v_cvt_pk_bf16_f32 v151, v151, v152
	v_cvt_pk_bf16_f32 v152, v131, v154
	v_mov_b64_e32 v[130:131], s[64:65]
	v_mul_f32_e32 v153, v125, v155
	v_mad_i64_i32 v[154:155], s[14:15], v148, s1, v[130:131]
	v_lshlrev_b64 v[132:133], 1, v[132:133]
	v_lshl_add_u64 v[154:155], v[154:155], 0, v[132:133]
	v_cvt_pk_bf16_f32 v153, v156, v153
	global_store_dwordx4 v[154:155], v[150:153], off nt sc1
	v_mul_f32_e32 v156, 0xbfb8aa3b, v98
	v_exp_f32_e32 v156, v156
	v_mul_f32_e32 v151, 0xbfb8aa3b, v90
	v_mul_f32_e32 v152, 0xbfb8aa3b, v99
	v_exp_f32_e32 v151, v151
	v_exp_f32_e32 v152, v152
	v_mul_f32_e32 v153, 0xbfb8aa3b, v91
	v_exp_f32_e32 v153, v153
	v_add_f32_e32 v151, 1.0, v151
	v_add_f32_e32 v152, 1.0, v152
	v_rcp_f32_e32 v151, v151
	v_rcp_f32_e32 v152, v152
	v_add_f32_e32 v150, 1.0, v156
	v_mul_f32_e32 v155, 0xbfb8aa3b, v92
	v_mul_f32_e32 v154, v110, v151
	v_mul_f32_e32 v151, v119, v152
	v_add_f32_e32 v152, 1.0, v153
	v_mul_f32_e32 v153, 0xbfb8aa3b, v100
	v_mul_f32_e32 v156, 0xbfb8aa3b, v101
	v_exp_f32_e32 v153, v153
	v_exp_f32_e32 v155, v155
	v_exp_f32_e32 v156, v156
	v_mul_f32_e32 v157, 0xbfb8aa3b, v93
	v_exp_f32_e32 v157, v157
	v_rcp_f32_e32 v150, v150
	v_rcp_f32_e32 v152, v152
	v_add_f32_e32 v153, 1.0, v153
	v_add_f32_e32 v155, 1.0, v155
	v_add_f32_e32 v156, 1.0, v156
	v_rcp_f32_e32 v153, v153
	v_rcp_f32_e32 v155, v155
	v_rcp_f32_e32 v156, v156
	v_add_f32_e32 v157, 1.0, v157
	v_rcp_f32_e32 v157, v157
	v_mul_f32_e32 v150, v118, v150
	v_mul_f32_e32 v152, v111, v152
	v_mul_f32_e32 v153, v120, v153
	v_mul_f32_e32 v155, v112, v155
	v_mul_f32_e32 v156, v121, v156
	v_cvt_pk_bf16_f32 v150, v150, v151
	v_cvt_pk_bf16_f32 v151, v153, v156
	v_cvt_pk_bf16_f32 v152, v154, v152
	v_mul_f32_e32 v154, 0xbfb8aa3b, v82
	v_mul_f32_e32 v157, v113, v157
	v_cvt_pk_bf16_f32 v153, v155, v157
	v_exp_f32_e32 v156, v154
	v_mad_i64_i32 v[154:155], s[14:15], v147, s1, v[130:131]
	v_lshl_add_u64 v[154:155], v[154:155], 0, v[132:133]
	global_store_dwordx4 v[154:155], v[150:153], off nt sc1
	v_mul_f32_e32 v155, 0xbfb8aa3b, v76
	v_exp_f32_e32 v155, v155
	v_mul_f32_e32 v151, 0xbfb8aa3b, v74
	v_mul_f32_e32 v152, 0xbfb8aa3b, v83
	v_exp_f32_e32 v151, v151
	v_exp_f32_e32 v152, v152
	v_mul_f32_e32 v153, 0xbfb8aa3b, v75
	v_exp_f32_e32 v153, v153
	v_add_f32_e32 v151, 1.0, v151
	v_add_f32_e32 v152, 1.0, v152
	v_rcp_f32_e32 v151, v151
	v_rcp_f32_e32 v152, v152
	v_add_f32_e32 v150, 1.0, v156
	v_mul_f32_e32 v156, 0xbfb8aa3b, v85
	v_mul_f32_e32 v154, v94, v151
	v_mul_f32_e32 v151, v103, v152
	v_add_f32_e32 v152, 1.0, v153
	v_mul_f32_e32 v153, 0xbfb8aa3b, v84
	v_exp_f32_e32 v153, v153
	v_exp_f32_e32 v156, v156
	v_mul_f32_e32 v157, 0xbfb8aa3b, v77
	v_exp_f32_e32 v157, v157
	v_rcp_f32_e32 v150, v150
	v_rcp_f32_e32 v152, v152
	v_add_f32_e32 v153, 1.0, v153
	v_add_f32_e32 v155, 1.0, v155
	v_add_f32_e32 v156, 1.0, v156
	v_rcp_f32_e32 v153, v153
	v_rcp_f32_e32 v155, v155
	v_rcp_f32_e32 v156, v156
	v_add_f32_e32 v157, 1.0, v157
	v_rcp_f32_e32 v157, v157
	v_mul_f32_e32 v150, v102, v150
	v_mul_f32_e32 v152, v95, v152
	v_mul_f32_e32 v153, v104, v153
	v_mul_f32_e32 v155, v96, v155
	v_mul_f32_e32 v156, v105, v156
	v_cvt_pk_bf16_f32 v150, v150, v151
	v_cvt_pk_bf16_f32 v151, v153, v156
	v_cvt_pk_bf16_f32 v152, v154, v152
	v_mul_f32_e32 v154, 0xbfb8aa3b, v70
	v_mul_f32_e32 v157, v97, v157
	v_cvt_pk_bf16_f32 v153, v155, v157
	v_exp_f32_e32 v156, v154
	v_mad_i64_i32 v[154:155], s[14:15], v146, s1, v[130:131]
	v_lshl_add_u64 v[154:155], v[154:155], 0, v[132:133]
	global_store_dwordx4 v[154:155], v[150:153], off nt sc1
	v_mul_f32_e32 v155, 0xbfb8aa3b, v68
	v_exp_f32_e32 v155, v155
	v_mul_f32_e32 v151, 0xbfb8aa3b, v66
	v_mul_f32_e32 v152, 0xbfb8aa3b, v71
	v_exp_f32_e32 v151, v151
	v_exp_f32_e32 v152, v152
	v_mul_f32_e32 v153, 0xbfb8aa3b, v67
	v_exp_f32_e32 v153, v153
	v_add_f32_e32 v151, 1.0, v151
	v_add_f32_e32 v152, 1.0, v152
	v_rcp_f32_e32 v151, v151
	v_rcp_f32_e32 v152, v152
	v_add_f32_e32 v150, 1.0, v156
	v_mul_f32_e32 v156, 0xbfb8aa3b, v73
	v_mul_f32_e32 v154, v78, v151
	v_mul_f32_e32 v151, v87, v152
	v_add_f32_e32 v152, 1.0, v153
	v_mul_f32_e32 v153, 0xbfb8aa3b, v72
	v_exp_f32_e32 v153, v153
	v_exp_f32_e32 v156, v156
	v_mul_f32_e32 v157, 0xbfb8aa3b, v69
	v_exp_f32_e32 v157, v157
	v_rcp_f32_e32 v150, v150
	v_rcp_f32_e32 v152, v152
	v_add_f32_e32 v153, 1.0, v153
	v_add_f32_e32 v155, 1.0, v155
	v_add_f32_e32 v156, 1.0, v156
	v_rcp_f32_e32 v153, v153
	v_rcp_f32_e32 v155, v155
	v_rcp_f32_e32 v156, v156
	v_add_f32_e32 v157, 1.0, v157
	v_rcp_f32_e32 v157, v157
	v_mul_f32_e32 v150, v86, v150
	v_mul_f32_e32 v152, v79, v152
	v_mul_f32_e32 v153, v88, v153
	v_mul_f32_e32 v155, v80, v155
	v_mul_f32_e32 v156, v89, v156
	v_cvt_pk_bf16_f32 v150, v150, v151
	v_cvt_pk_bf16_f32 v151, v153, v156
	v_cvt_pk_bf16_f32 v152, v154, v152
	v_mul_f32_e32 v154, 0xbfb8aa3b, v48
	v_mul_f32_e32 v157, v81, v157
	v_cvt_pk_bf16_f32 v153, v155, v157
	v_exp_f32_e32 v156, v154
	v_mad_i64_i32 v[154:155], s[14:15], v145, s1, v[130:131]
	v_lshl_add_u64 v[154:155], v[154:155], 0, v[132:133]
	global_store_dwordx4 v[154:155], v[150:153], off nt sc1
	v_mul_f32_e32 v155, 0xbfb8aa3b, v42
	v_exp_f32_e32 v155, v155
	v_mul_f32_e32 v151, 0xbfb8aa3b, v40
	v_mul_f32_e32 v152, 0xbfb8aa3b, v49
	v_exp_f32_e32 v151, v151
	v_exp_f32_e32 v152, v152
	v_mul_f32_e32 v153, 0xbfb8aa3b, v41
	v_exp_f32_e32 v153, v153
	v_add_f32_e32 v151, 1.0, v151
	v_add_f32_e32 v152, 1.0, v152
	v_rcp_f32_e32 v151, v151
	v_rcp_f32_e32 v152, v152
	v_add_f32_e32 v150, 1.0, v156
	v_mul_f32_e32 v156, 0xbfb8aa3b, v51
	v_mul_f32_e32 v154, v56, v151
	v_mul_f32_e32 v151, v61, v152
	v_add_f32_e32 v152, 1.0, v153
	v_mul_f32_e32 v153, 0xbfb8aa3b, v50
	v_exp_f32_e32 v153, v153
	v_exp_f32_e32 v156, v156
	v_mul_f32_e32 v157, 0xbfb8aa3b, v43
	v_exp_f32_e32 v157, v157
	v_rcp_f32_e32 v150, v150
	v_rcp_f32_e32 v152, v152
	v_add_f32_e32 v153, 1.0, v153
	v_add_f32_e32 v155, 1.0, v155
	v_add_f32_e32 v156, 1.0, v156
	v_rcp_f32_e32 v153, v153
	v_rcp_f32_e32 v155, v155
	v_rcp_f32_e32 v156, v156
	v_add_f32_e32 v157, 1.0, v157
	v_rcp_f32_e32 v157, v157
	v_mul_f32_e32 v150, v60, v150
	v_mul_f32_e32 v152, v57, v152
	v_mul_f32_e32 v153, v62, v153
	v_mul_f32_e32 v155, v58, v155
	v_mul_f32_e32 v156, v63, v156
	v_cvt_pk_bf16_f32 v150, v150, v151
	v_cvt_pk_bf16_f32 v151, v153, v156
	v_cvt_pk_bf16_f32 v152, v154, v152
	v_mul_f32_e32 v154, 0xbfb8aa3b, v32
	v_mul_f32_e32 v157, v59, v157
	v_cvt_pk_bf16_f32 v153, v155, v157
	v_exp_f32_e32 v156, v154
	v_mad_i64_i32 v[154:155], s[14:15], v144, s1, v[130:131]
	v_lshl_add_u64 v[154:155], v[154:155], 0, v[132:133]
	global_store_dwordx4 v[154:155], v[150:153], off nt sc1
	v_mul_f32_e32 v155, 0xbfb8aa3b, v26
	v_exp_f32_e32 v155, v155
	v_mul_f32_e32 v151, 0xbfb8aa3b, v24
	v_mul_f32_e32 v152, 0xbfb8aa3b, v33
	v_exp_f32_e32 v151, v151
	v_exp_f32_e32 v152, v152
	v_mul_f32_e32 v153, 0xbfb8aa3b, v25
	v_exp_f32_e32 v153, v153
	v_add_f32_e32 v151, 1.0, v151
	v_add_f32_e32 v152, 1.0, v152
	v_rcp_f32_e32 v151, v151
	v_rcp_f32_e32 v152, v152
	v_add_f32_e32 v150, 1.0, v156
	v_mul_f32_e32 v156, 0xbfb8aa3b, v35
	v_mul_f32_e32 v154, v44, v151
	v_mul_f32_e32 v151, v53, v152
	v_add_f32_e32 v152, 1.0, v153
	v_mul_f32_e32 v153, 0xbfb8aa3b, v34
	v_exp_f32_e32 v153, v153
	v_exp_f32_e32 v156, v156
	v_mul_f32_e32 v157, 0xbfb8aa3b, v27
	v_exp_f32_e32 v157, v157
	v_rcp_f32_e32 v150, v150
	v_rcp_f32_e32 v152, v152
	v_add_f32_e32 v153, 1.0, v153
	v_add_f32_e32 v155, 1.0, v155
	v_add_f32_e32 v156, 1.0, v156
	v_rcp_f32_e32 v153, v153
	v_rcp_f32_e32 v155, v155
	v_rcp_f32_e32 v156, v156
	v_add_f32_e32 v157, 1.0, v157
	v_rcp_f32_e32 v157, v157
	v_mul_f32_e32 v150, v52, v150
	v_mul_f32_e32 v152, v45, v152
	v_mul_f32_e32 v153, v54, v153
	v_mul_f32_e32 v155, v46, v155
	v_mul_f32_e32 v156, v55, v156
	v_cvt_pk_bf16_f32 v150, v150, v151
	v_cvt_pk_bf16_f32 v151, v153, v156
	v_cvt_pk_bf16_f32 v152, v154, v152
	v_mul_f32_e32 v154, 0xbfb8aa3b, v16
	v_mul_f32_e32 v157, v47, v157
	v_cvt_pk_bf16_f32 v153, v155, v157
	v_exp_f32_e32 v156, v154
	v_mad_i64_i32 v[154:155], s[14:15], v143, s1, v[130:131]
	v_lshl_add_u64 v[154:155], v[154:155], 0, v[132:133]
	global_store_dwordx4 v[154:155], v[150:153], off nt sc1
	v_mul_f32_e32 v155, 0xbfb8aa3b, v10
	v_exp_f32_e32 v155, v155
	v_mul_f32_e32 v151, 0xbfb8aa3b, v8
	v_mul_f32_e32 v152, 0xbfb8aa3b, v17
	v_exp_f32_e32 v151, v151
	v_exp_f32_e32 v152, v152
	v_mul_f32_e32 v153, 0xbfb8aa3b, v9
	v_exp_f32_e32 v153, v153
	v_add_f32_e32 v151, 1.0, v151
	v_add_f32_e32 v152, 1.0, v152
	v_rcp_f32_e32 v151, v151
	v_rcp_f32_e32 v152, v152
	v_add_f32_e32 v150, 1.0, v156
	v_mul_f32_e32 v156, 0xbfb8aa3b, v19
	v_mul_f32_e32 v154, v28, v151
	v_mul_f32_e32 v151, v37, v152
	v_add_f32_e32 v152, 1.0, v153
	v_mul_f32_e32 v153, 0xbfb8aa3b, v18
	v_exp_f32_e32 v153, v153
	v_exp_f32_e32 v156, v156
	v_mul_f32_e32 v157, 0xbfb8aa3b, v11
	v_exp_f32_e32 v157, v157
	v_rcp_f32_e32 v150, v150
	v_rcp_f32_e32 v152, v152
	v_add_f32_e32 v153, 1.0, v153
	v_add_f32_e32 v155, 1.0, v155
	v_add_f32_e32 v156, 1.0, v156
	v_rcp_f32_e32 v153, v153
	v_rcp_f32_e32 v155, v155
	v_rcp_f32_e32 v156, v156
	v_add_f32_e32 v157, 1.0, v157
	v_rcp_f32_e32 v157, v157
	v_mul_f32_e32 v150, v36, v150
	v_mul_f32_e32 v152, v29, v152
	v_mul_f32_e32 v153, v38, v153
	v_mul_f32_e32 v155, v30, v155
	v_mul_f32_e32 v156, v39, v156
	v_cvt_pk_bf16_f32 v150, v150, v151
	v_cvt_pk_bf16_f32 v151, v153, v156
	v_cvt_pk_bf16_f32 v152, v154, v152
	v_mul_f32_e32 v154, 0xbfb8aa3b, v4
	v_mul_f32_e32 v157, v31, v157
	v_cvt_pk_bf16_f32 v153, v155, v157
	v_exp_f32_e32 v156, v154
	v_mad_i64_i32 v[154:155], s[14:15], v142, s1, v[130:131]
	v_lshl_add_u64 v[154:155], v[154:155], 0, v[132:133]
	global_store_dwordx4 v[154:155], v[150:153], off nt sc1
	v_mul_f32_e32 v155, 0xbfb8aa3b, v2
	v_mul_f32_e32 v157, 0xbfb8aa3b, v3
	v_mul_f32_e32 v151, 0xbfb8aa3b, v0
	v_mul_f32_e32 v152, 0xbfb8aa3b, v5
	v_exp_f32_e32 v151, v151
	v_exp_f32_e32 v152, v152
	v_mul_f32_e32 v153, 0xbfb8aa3b, v1
	v_exp_f32_e32 v153, v153
	v_add_f32_e32 v151, 1.0, v151
	v_add_f32_e32 v152, 1.0, v152
	v_rcp_f32_e32 v151, v151
	v_rcp_f32_e32 v152, v152
	v_add_f32_e32 v150, 1.0, v156
	v_mul_f32_e32 v156, 0xbfb8aa3b, v7
	v_mul_f32_e32 v154, v12, v151
	v_mul_f32_e32 v151, v21, v152
	v_add_f32_e32 v152, 1.0, v153
	v_mul_f32_e32 v153, 0xbfb8aa3b, v6
	v_exp_f32_e32 v153, v153
	v_exp_f32_e32 v155, v155
	v_exp_f32_e32 v156, v156
	v_exp_f32_e32 v157, v157
	v_add_f32_e32 v153, 1.0, v153
	v_rcp_f32_e32 v150, v150
	v_rcp_f32_e32 v152, v152
	v_rcp_f32_e32 v153, v153
	v_add_f32_e32 v155, 1.0, v155
	v_add_f32_e32 v156, 1.0, v156
	v_add_f32_e32 v157, 1.0, v157
	v_rcp_f32_e32 v155, v155
	v_rcp_f32_e32 v156, v156
	v_rcp_f32_e32 v157, v157
	v_mad_i64_i32 v[130:131], s[14:15], v64, s1, v[130:131]
	v_mul_f32_e32 v150, v20, v150
	v_mul_f32_e32 v152, v13, v152
	v_mul_f32_e32 v153, v22, v153
	v_lshl_add_u64 v[130:131], v[130:131], 0, v[132:133]
	v_mul_f32_e32 v155, v14, v155
	v_mul_f32_e32 v156, v23, v156
	v_mul_f32_e32 v157, v15, v157
	v_cvt_pk_bf16_f32 v150, v150, v151
	v_cvt_pk_bf16_f32 v151, v153, v156
	v_cvt_pk_bf16_f32 v152, v154, v152
	v_cvt_pk_bf16_f32 v153, v155, v157
	global_store_dwordx4 v[130:131], v[150:153], off nt sc1
	s_mov_b32 s99, 1
	s_cbranch_execnz .LBB0_360
.LBB0_362:
	s_lshl_b32 s14, s31, 8
	s_or_b32 s14, s14, s26
	v_add_u32_e32 v130, s14, v149
	v_ashrrev_i32_e32 v131, 31, v130
	v_mov_b64_e32 v[132:133], s[64:65]
	v_mad_i64_i32 v[148:149], s[14:15], v148, s1, v[132:133]
	v_lshlrev_b64 v[130:131], 1, v[130:131]
	v_lshl_add_u64 v[148:149], v[148:149], 0, v[130:131]
	v_cvt_pk_bf16_f32 v126, v126, v127
	v_cvt_pk_bf16_f32 v127, v128, v129
	v_cvt_pk_bf16_f32 v128, v122, v123
	v_cvt_pk_bf16_f32 v129, v124, v125
	global_store_dwordx4 v[148:149], v[126:129], off nt sc1
	v_cvt_pk_bf16_f32 v114, v114, v115
	v_cvt_pk_bf16_f32 v115, v116, v117
	v_cvt_pk_bf16_f32 v116, v106, v107
	v_mad_i64_i32 v[106:107], s[14:15], v147, s1, v[132:133]
	v_cvt_pk_bf16_f32 v117, v108, v109
	global_store_dwordx4 v[148:149], v[114:117], off offset:256 nt sc1
	s_nop 1
	v_lshl_add_u64 v[114:115], v[106:107], 0, v[130:131]
	v_cvt_pk_bf16_f32 v106, v118, v119
	v_cvt_pk_bf16_f32 v107, v120, v121
	v_cvt_pk_bf16_f32 v108, v110, v111
	v_cvt_pk_bf16_f32 v109, v112, v113
	global_store_dwordx4 v[114:115], v[106:109], off nt sc1
	v_cvt_pk_bf16_f32 v98, v98, v99
	v_cvt_pk_bf16_f32 v99, v100, v101
	v_cvt_pk_bf16_f32 v100, v90, v91
	v_mad_i64_i32 v[90:91], s[14:15], v146, s1, v[132:133]
	v_cvt_pk_bf16_f32 v101, v92, v93
	global_store_dwordx4 v[114:115], v[98:101], off offset:256 nt sc1
	s_nop 1
	v_lshl_add_u64 v[98:99], v[90:91], 0, v[130:131]
	v_cvt_pk_bf16_f32 v90, v102, v103
	v_cvt_pk_bf16_f32 v91, v104, v105
	v_cvt_pk_bf16_f32 v92, v94, v95
	v_cvt_pk_bf16_f32 v93, v96, v97
	global_store_dwordx4 v[98:99], v[90:93], off nt sc1
	v_cvt_pk_bf16_f32 v82, v82, v83
	v_cvt_pk_bf16_f32 v83, v84, v85
	v_cvt_pk_bf16_f32 v84, v74, v75
	v_mad_i64_i32 v[74:75], s[14:15], v145, s1, v[132:133]
	v_cvt_pk_bf16_f32 v85, v76, v77
	global_store_dwordx4 v[98:99], v[82:85], off offset:256 nt sc1
	s_nop 1
	v_lshl_add_u64 v[82:83], v[74:75], 0, v[130:131]
	v_cvt_pk_bf16_f32 v74, v86, v87
	v_cvt_pk_bf16_f32 v75, v88, v89
	v_cvt_pk_bf16_f32 v76, v78, v79
	v_cvt_pk_bf16_f32 v77, v80, v81
	global_store_dwordx4 v[82:83], v[74:77], off nt sc1
	v_cvt_pk_bf16_f32 v70, v70, v71
	v_cvt_pk_bf16_f32 v71, v72, v73
	v_cvt_pk_bf16_f32 v72, v66, v67
	v_mad_i64_i32 v[66:67], s[14:15], v144, s1, v[132:133]
	v_lshl_add_u64 v[66:67], v[66:67], 0, v[130:131]
	v_cvt_pk_bf16_f32 v73, v68, v69
	global_store_dwordx4 v[82:83], v[70:73], off offset:256 nt sc1
	v_cvt_pk_bf16_f32 v60, v60, v61
	v_cvt_pk_bf16_f32 v61, v62, v63
	v_cvt_pk_bf16_f32 v62, v56, v57
	v_cvt_pk_bf16_f32 v63, v58, v59
	global_store_dwordx4 v[66:67], v[60:63], off nt sc1
	v_cvt_pk_bf16_f32 v48, v48, v49
	v_cvt_pk_bf16_f32 v49, v50, v51
	v_cvt_pk_bf16_f32 v50, v40, v41
	v_mad_i64_i32 v[40:41], s[14:15], v143, s1, v[132:133]
	v_cvt_pk_bf16_f32 v51, v42, v43
	global_store_dwordx4 v[66:67], v[48:51], off offset:256 nt sc1
	s_nop 1
	v_lshl_add_u64 v[48:49], v[40:41], 0, v[130:131]
	v_cvt_pk_bf16_f32 v40, v52, v53
	v_cvt_pk_bf16_f32 v41, v54, v55
	v_cvt_pk_bf16_f32 v42, v44, v45
	v_cvt_pk_bf16_f32 v43, v46, v47
	global_store_dwordx4 v[48:49], v[40:43], off nt sc1
	v_cvt_pk_bf16_f32 v32, v32, v33
	v_cvt_pk_bf16_f32 v33, v34, v35
	v_cvt_pk_bf16_f32 v34, v24, v25
	v_mad_i64_i32 v[24:25], s[14:15], v142, s1, v[132:133]
	v_cvt_pk_bf16_f32 v35, v26, v27
	global_store_dwordx4 v[48:49], v[32:35], off offset:256 nt sc1
	s_nop 1
	v_lshl_add_u64 v[32:33], v[24:25], 0, v[130:131]
	v_cvt_pk_bf16_f32 v24, v36, v37
	v_cvt_pk_bf16_f32 v25, v38, v39
	v_cvt_pk_bf16_f32 v26, v28, v29
	v_cvt_pk_bf16_f32 v27, v30, v31
	global_store_dwordx4 v[32:33], v[24:27], off nt sc1
	v_cvt_pk_bf16_f32 v16, v16, v17
	v_cvt_pk_bf16_f32 v17, v18, v19
	v_cvt_pk_bf16_f32 v18, v8, v9
	v_mad_i64_i32 v[8:9], s[14:15], v64, s1, v[132:133]
	v_cvt_pk_bf16_f32 v19, v10, v11
	global_store_dwordx4 v[32:33], v[16:19], off offset:256 nt sc1
	s_nop 1
	v_lshl_add_u64 v[16:17], v[8:9], 0, v[130:131]
	v_cvt_pk_bf16_f32 v8, v20, v21
	v_cvt_pk_bf16_f32 v9, v22, v23
	v_cvt_pk_bf16_f32 v10, v12, v13
	v_cvt_pk_bf16_f32 v11, v14, v15
	global_store_dwordx4 v[16:17], v[8:11], off nt sc1
	v_cvt_pk_bf16_f32 v4, v4, v5
	v_cvt_pk_bf16_f32 v5, v6, v7
	v_cvt_pk_bf16_f32 v6, v0, v1
	v_cvt_pk_bf16_f32 v7, v2, v3
	global_store_dwordx4 v[16:17], v[4:7], off offset:256 nt sc1
	s_mov_b32 s99, 2
	s_cmp_eq_u32 s31, 10
	s_mov_b64 s[14:15], -1
	s_cbranch_scc1 .LBB0_353

.LBB0_665:
	s_mov_b32 s99, 0
	v_readlane_b32 s6, v254, 12
	s_waitcnt vmcnt(63) expcnt(7) lgkmcnt(15)
	s_lshl_b32 s21, s45, 20
	s_lshl_b32 s20, s6, 6
	s_mov_b64 s[6:7], -1
	s_and_b64 vcc, exec, s[50:51]
	v_mbcnt_lo_u32_b32 v0, -1, 0
	v_mbcnt_hi_u32_b32 v0, -1, v0
	s_cbranch_vccz .LBB0_679
	v_mbcnt_lo_u32_b32 v0, -1, 0
	v_mbcnt_hi_u32_b32 v0, -1, v0
	v_mov_b32_e32 v8, 1
	v_add_u32_e32 v1, s20, v0
	v_ashrrev_i32_e32 v3, 31, v1
	v_lshrrev_b32_e32 v3, 26, v3
	v_readfirstlane_b32 s10, v1
	v_lshlrev_b32_e32 v2, 4, v1
	v_add_u32_e32 v3, v1, v3
	v_bfe_i32 v1, v1, 27, 1
	v_lshrrev_b32_e32 v1, 22, v1
	v_add_u32_e32 v1, v2, v1
	v_and_b32_e32 v1, 0xfffffc00, v1
	v_sub_u32_e32 v1, v2, v1
	v_lshrrev_b32_e32 v4, 4, v1
	v_bitop3_b32 v1, v4, v1, 32 bitop3:0x6c
	v_ashrrev_i32_e32 v5, 31, v1
	v_ashrrev_i32_e32 v3, 6, v3
	v_lshrrev_b32_e32 v5, 26, v5
	v_lshlrev_b32_e32 v4, 3, v3
	v_add_u32_e32 v5, v1, v5
	v_and_b32_e32 v4, -16, v4
	v_ashrrev_i32_e32 v6, 6, v5
	v_and_b32_e32 v5, 0xc0, v5
	v_add_u32_e32 v4, v6, v4
	v_sub_u32_e32 v1, v1, v5
	v_lshlrev_b32_e32 v3, 5, v3
	v_ashrrev_i16_sdwa v1, v8, sext(v1) dst_sel:DWORD dst_unused:UNUSED_PAD src0_sel:DWORD src1_sel:BYTE_0
	v_lshlrev_b32_e32 v5, 1, v4
	v_lshrrev_b32_e32 v7, 2, v4
	v_and_b32_e32 v6, 3, v6
	s_mov_b32 s11, 0x3fffe0
	v_and_b32_e32 v3, 32, v3
	v_bfe_i32 v1, v1, 0, 16
	v_and_b32_e32 v5, 24, v5
	v_and_b32_e32 v7, 4, v7
	v_and_or_b32 v6, v4, s11, v6
	v_or3_b32 v5, v6, v7, v5
	v_add_lshl_u32 v1, v3, v1, 1
	v_lshl_add_u32 v132, v4, 10, v1
	v_lshl_add_u32 v133, v5, 10, v1
	v_add_u32_e32 v1, 0x2000, v2
	v_ashrrev_i32_e32 v2, 31, v1
	v_lshrrev_b32_e32 v2, 22, v2
	v_add_u32_e32 v2, v1, v2
	v_ashrrev_i32_e32 v2, 10, v2
	v_mul_i32_i24_e32 v3, 0x400, v2
	v_sub_u32_e32 v1, v1, v3
	v_lshrrev_b32_e32 v3, 4, v1
	v_bitop3_b32 v1, v3, v1, 32 bitop3:0x6c
	v_ashrrev_i32_e32 v4, 31, v1
	v_lshrrev_b32_e32 v4, 26, v4
	v_readlane_b32 s6, v254, 10
	v_lshlrev_b32_e32 v3, 3, v2
	v_add_u32_e32 v4, v1, v4
	s_add_u32 s6, s6, s21
	v_readlane_b32 s7, v254, 11
	v_and_b32_e32 v3, -16, v3
	v_ashrrev_i32_e32 v5, 6, v4
	v_and_b32_e32 v4, 0xc0, v4
	s_addc_u32 s7, s7, 0
	v_add_u32_e32 v3, v5, v3
	v_sub_u32_e32 v1, v1, v4
	s_add_u32 s8, s6, 0x20000
	v_lshlrev_b32_e32 v2, 5, v2
	v_ashrrev_i16_sdwa v1, v8, sext(v1) dst_sel:DWORD dst_unused:UNUSED_PAD src0_sel:DWORD src1_sel:BYTE_0
	v_lshlrev_b32_e32 v4, 1, v3
	v_lshrrev_b32_e32 v6, 2, v3
	v_and_b32_e32 v5, 3, v5
	s_addc_u32 s9, s7, 0
	v_and_b32_e32 v2, 32, v2
	v_bfe_i32 v1, v1, 0, 16
	v_and_b32_e32 v4, 24, v4
	v_and_b32_e32 v6, 4, v6
	v_and_or_b32 v5, v3, s11, v5
	s_ashr_i32 s11, s10, 6
	v_or3_b32 v4, v5, v6, v4
	v_add_lshl_u32 v1, v2, v1, 1
	s_lshl_b32 s22, s11, 10
	v_lshl_add_u32 v134, v3, 10, v1
	v_lshl_add_u32 v135, v4, 10, v1
	s_add_i32 s23, s22, 0
	v_mov_b32_e32 v1, v133
	s_add_i32 m0, s23, 0x10000
	s_add_i32 s24, s23, 0x2000
	global_load_lds_dwordx4 v1, s[6:7]
	v_mov_b32_e32 v1, v135
	s_add_i32 m0, s23, 0x12000
	s_add_i32 s25, s23, 0x4000
	global_load_lds_dwordx4 v1, s[6:7]
	v_mov_b32_e32 v1, v133
	s_add_i32 m0, s23, 0x14000
	s_add_i32 s26, s23, 0x6000
	global_load_lds_dwordx4 v1, s[8:9]
	v_mov_b32_e32 v1, v135
	s_add_i32 m0, s23, 0x16000
	s_ashr_i32 s12, s10, 8
	global_load_lds_dwordx4 v1, s[8:9]
	v_mov_b32_e32 v1, v132
	s_mov_b32 m0, s23
	v_readlane_b32 s8, v254, 40
	global_load_lds_dwordx4 v1, s[88:89]
	v_mov_b32_e32 v1, v134
	s_mov_b32 m0, s24
	v_readlane_b32 s9, v254, 41
	global_load_lds_dwordx4 v1, s[88:89]
	v_mov_b32_e32 v1, v132
	s_mov_b32 m0, s25
	s_cmp_eq_u32 s12, 1
	s_nop 0
	global_load_lds_dwordx4 v1, s[8:9]
	v_mov_b32_e32 v1, v134
	s_mov_b32 m0, s26
	s_nop 0
	global_load_lds_dwordx4 v1, s[8:9]
	s_cselect_b64 s[8:9], -1, 0
	s_cmp_lg_u32 s12, 1
	s_cbranch_scc1 .LBB0_668
	s_barrier

.LBB0_672:
	s_add_u32 s16, s14, 0xfffe0080
	s_addc_u32 s17, s15, -1
	s_add_i32 s49, 0, 0x10000
	s_cmp_eq_u32 s39, 4
	s_cselect_b32 s17, s89, s17
	s_cselect_b32 s16, s88, s16
	v_add_u32_e32 v64, s49, v138
	s_cselect_b32 s19, s35, s38
	s_cselect_b32 s18, s36, s37
	s_add_i32 s56, 0, 0x14000
	ds_read_b128 v[140:143], v64
	ds_read_b128 v[144:147], v64 offset:1024
	ds_read_b128 v[148:151], v64 offset:2048
	ds_read_b128 v[152:155], v64 offset:3072
	v_add_u32_e32 v64, s56, v138
	ds_read_b128 v[156:159], v64
	ds_read_b128 v[160:163], v64 offset:1024
	ds_read_b128 v[164:167], v64 offset:2048
	ds_read_b128 v[168:171], v64 offset:3072
	v_mov_b32_e32 v64, v132
	ds_read_b128 v[172:175], v139
	ds_read_b128 v[176:179], v139 offset:1024
	ds_read_b128 v[180:183], v139 offset:2048
	ds_read_b128 v[184:187], v139 offset:3072
	ds_read_b128 v[188:191], v139 offset:4096
	ds_read_b128 v[192:195], v139 offset:5120
	ds_read_b128 v[196:199], v139 offset:6144
	ds_read_b128 v[200:203], v139 offset:7168
	s_add_i32 m0, s23, 0xc000
	s_nop 0
	global_load_lds_dwordx4 v64, s[14:15]
	v_mov_b32_e32 v64, v134
	s_add_i32 m0, s23, 0xe000
	s_nop 0
	global_load_lds_dwordx4 v64, s[14:15]
	s_cmp_eq_u32 s99, 0
	s_cbranch_scc1 .Lrw_oa1_n
	s_waitcnt vmcnt(24)
	s_branch .Lrw_oa1_d

.Lrw_oa1_d:
	s_waitcnt lgkmcnt(0)
	s_barrier
	s_setprio 1
	s_waitcnt lgkmcnt(0)
	v_mfma_f32_16x16x128_f8f6f4 v[126:129], v[140:147], v[172:179], v[126:129]
	v_mfma_f32_16x16x128_f8f6f4 v[122:125], v[148:155], v[172:179], v[122:125]
	v_mfma_f32_16x16x128_f8f6f4 v[114:117], v[140:147], v[180:187], v[114:117]
	v_mfma_f32_16x16x128_f8f6f4 v[106:109], v[148:155], v[180:187], v[106:109]
	v_mfma_f32_16x16x128_f8f6f4 v[98:101], v[140:147], v[188:195], v[98:101]
	v_mfma_f32_16x16x128_f8f6f4 v[204:207], v[148:155], v[188:195], v[90:93]
	v_mfma_f32_16x16x128_f8f6f4 v[208:211], v[140:147], v[196:203], v[82:85]
	v_mfma_f32_16x16x128_f8f6f4 v[212:215], v[148:155], v[196:203], v[74:77]
	s_setprio 0
	s_setprio 1
	v_mfma_f32_16x16x128_f8f6f4 v[118:121], v[156:163], v[172:179], v[118:121]
	v_mfma_f32_16x16x128_f8f6f4 v[110:113], v[164:171], v[172:179], v[110:113]
	v_mfma_f32_16x16x128_f8f6f4 v[102:105], v[156:163], v[180:187], v[102:105]
	v_mfma_f32_16x16x128_f8f6f4 v[172:175], v[164:171], v[180:187], v[94:97]
	v_mfma_f32_16x16x128_f8f6f4 v[176:179], v[156:163], v[188:195], v[86:89]
	v_mfma_f32_16x16x128_f8f6f4 v[180:183], v[164:171], v[188:195], v[78:81]
	v_mfma_f32_16x16x128_f8f6f4 v[184:187], v[156:163], v[196:203], v[70:73]
	v_mfma_f32_16x16x128_f8f6f4 v[188:191], v[164:171], v[196:203], v[66:69]
	s_setprio 0
	s_barrier
	v_mov_b32_e32 v64, v133
	s_add_i32 s49, s49, s22
	s_nop 2
	ds_read_b128 v[66:69], v139 offset:16384
	ds_read_b128 v[70:73], v139 offset:17408
	ds_read_b128 v[74:77], v139 offset:18432
	ds_read_b128 v[78:81], v139 offset:19456
	ds_read_b128 v[82:85], v139 offset:20480
	ds_read_b128 v[86:89], v139 offset:21504
	ds_read_b128 v[90:93], v139 offset:22528
	ds_read_b128 v[94:97], v139 offset:23552
	s_mov_b32 m0, s49
	s_nop 0
	global_load_lds_dwordx4 v64, s[18:19]
	v_mov_b32_e32 v64, v135
	s_add_i32 m0, s49, 0x2000
	s_add_u32 s50, s18, 0x20000
	global_load_lds_dwordx4 v64, s[18:19]
	s_addc_u32 s51, s19, 0
	v_mov_b32_e32 v64, v133
	s_add_i32 s49, s56, s22
	s_mov_b32 m0, s49
	s_nop 0
	global_load_lds_dwordx4 v64, s[50:51]
	v_mov_b32_e32 v64, v135
	s_add_i32 m0, s49, 0x2000
	s_nop 0
	global_load_lds_dwordx4 v64, s[50:51]
	v_mov_b32_e32 v64, v132
	s_mov_b32 m0, s23
	s_nop 0
	global_load_lds_dwordx4 v64, s[16:17]
	v_mov_b32_e32 v64, v134
	s_mov_b32 m0, s24
	s_nop 0
	global_load_lds_dwordx4 v64, s[16:17]
	s_cmp_eq_u32 s99, 0
	s_cbranch_scc1 .Lrw_oa2_n
	s_waitcnt vmcnt(24)
	s_branch .Lrw_oa2_d

.Lrw_oa2_d:
	s_mov_b32 s99, 0
	s_waitcnt lgkmcnt(0)
	s_barrier
	s_setprio 1
	s_waitcnt lgkmcnt(0)
	v_mfma_f32_16x16x128_f8f6f4 v[60:63], v[140:147], v[66:73], v[60:63]
	v_mfma_f32_16x16x128_f8f6f4 v[56:59], v[148:155], v[66:73], v[56:59]
	v_mfma_f32_16x16x128_f8f6f4 v[48:51], v[140:147], v[74:81], v[48:51]
	v_mfma_f32_16x16x128_f8f6f4 v[192:195], v[148:155], v[74:81], v[40:43]
	v_mfma_f32_16x16x128_f8f6f4 v[196:199], v[140:147], v[82:89], v[32:35]
	v_mfma_f32_16x16x128_f8f6f4 v[200:203], v[148:155], v[82:89], v[24:27]
	v_mfma_f32_16x16x128_f8f6f4 v[216:219], v[140:147], v[90:97], v[16:19]
	v_mfma_f32_16x16x128_f8f6f4 v[220:223], v[148:155], v[90:97], v[8:11]
	s_setprio 0
	s_setprio 1
	v_mfma_f32_16x16x128_f8f6f4 v[52:55], v[156:163], v[66:73], v[52:55]
	v_mfma_f32_16x16x128_f8f6f4 v[224:227], v[164:171], v[66:73], v[44:47]
	v_mfma_f32_16x16x128_f8f6f4 v[230:233], v[156:163], v[74:81], v[36:39]
	v_mfma_f32_16x16x128_f8f6f4 v[234:237], v[164:171], v[74:81], v[28:31]
	v_mfma_f32_16x16x128_f8f6f4 v[238:241], v[156:163], v[82:89], v[20:23]
	v_mfma_f32_16x16x128_f8f6f4 v[242:245], v[164:171], v[82:89], v[12:15]
	v_mfma_f32_16x16x128_f8f6f4 v[246:249], v[156:163], v[90:97], v[4:7]
	v_mfma_f32_16x16x128_f8f6f4 v[250:253], v[164:171], v[90:97], v[0:3]
	s_setprio 0
	s_barrier
	s_add_i32 s49, 0, 0x18000
	s_add_i32 s56, 0, 0x1c000
	s_nop 0
	v_add_u32_e32 v12, s49, v138
	v_add_u32_e32 v16, s56, v138
	ds_read_b128 v[0:3], v12
	ds_read_b128 v[4:7], v12 offset:1024
	ds_read_b128 v[8:11], v12 offset:2048
	ds_read_b128 v[12:15], v12 offset:3072
	ds_read_b128 v[140:143], v16
	ds_read_b128 v[144:147], v16 offset:1024
	ds_read_b128 v[148:151], v16 offset:2048
	ds_read_b128 v[152:155], v16 offset:3072
	s_add_u32 s50, s16, 0x20000
	v_mov_b32_e32 v64, v132
	s_mov_b32 m0, s25
	ds_read_b128 v[16:19], v139 offset:32768
	ds_read_b128 v[20:23], v139 offset:33792
	ds_read_b128 v[24:27], v139 offset:34816
	ds_read_b128 v[28:31], v139 offset:35840
	ds_read_b128 v[32:35], v139 offset:36864
	ds_read_b128 v[36:39], v139 offset:37888
	ds_read_b128 v[40:43], v139 offset:38912
	ds_read_b128 v[44:47], v139 offset:39936
	s_addc_u32 s51, s17, 0
	s_nop 0
	global_load_lds_dwordx4 v64, s[50:51]
	v_mov_b32_e32 v64, v134
	s_mov_b32 m0, s26
	s_nop 0
	global_load_lds_dwordx4 v64, s[50:51]
	s_waitcnt vmcnt(8)
	s_waitcnt lgkmcnt(0)
	s_barrier
	s_setprio 1
	s_waitcnt lgkmcnt(0)
	v_mfma_f32_16x16x128_f8f6f4 v[126:129], v[0:7], v[16:23], v[126:129]
	v_mfma_f32_16x16x128_f8f6f4 v[122:125], v[8:15], v[16:23], v[122:125]
	v_mfma_f32_16x16x128_f8f6f4 v[114:117], v[0:7], v[24:31], v[114:117]
	v_mfma_f32_16x16x128_f8f6f4 v[106:109], v[8:15], v[24:31], v[106:109]
	v_mfma_f32_16x16x128_f8f6f4 v[98:101], v[0:7], v[32:39], v[98:101]
	v_mfma_f32_16x16x128_f8f6f4 v[90:93], v[8:15], v[32:39], v[204:207]
	v_mfma_f32_16x16x128_f8f6f4 v[82:85], v[0:7], v[40:47], v[208:211]
	v_mfma_f32_16x16x128_f8f6f4 v[74:77], v[8:15], v[40:47], v[212:215]
	s_setprio 0
	s_setprio 1
	v_mfma_f32_16x16x128_f8f6f4 v[118:121], v[140:147], v[16:23], v[118:121]
	v_mfma_f32_16x16x128_f8f6f4 v[110:113], v[148:155], v[16:23], v[110:113]
	v_mfma_f32_16x16x128_f8f6f4 v[102:105], v[140:147], v[24:31], v[102:105]
	v_mfma_f32_16x16x128_f8f6f4 v[94:97], v[148:155], v[24:31], v[172:175]
	v_mfma_f32_16x16x128_f8f6f4 v[86:89], v[140:147], v[32:39], v[176:179]
	v_mfma_f32_16x16x128_f8f6f4 v[78:81], v[148:155], v[32:39], v[180:183]
	v_mfma_f32_16x16x128_f8f6f4 v[70:73], v[140:147], v[40:47], v[184:187]
	v_mfma_f32_16x16x128_f8f6f4 v[66:69], v[148:155], v[40:47], v[188:191]
	s_setprio 0
	s_barrier
	v_mov_b32_e32 v64, v133
	ds_read_b128 v[156:159], v139 offset:49152
	ds_read_b128 v[160:163], v139 offset:50176
	ds_read_b128 v[164:167], v139 offset:51200
	ds_read_b128 v[168:171], v139 offset:52224
	ds_read_b128 v[172:175], v139 offset:53248
	ds_read_b128 v[176:179], v139 offset:54272
	ds_read_b128 v[180:183], v139 offset:55296
	ds_read_b128 v[184:187], v139 offset:56320
	s_add_i32 s49, s49, s22
	v_lshl_add_u64 v[16:17], s[18:19], 0, v[64:65]
	v_lshl_add_u64 v[16:17], v[16:17], 0, s[80:81]
	s_mov_b32 m0, s49
	v_mov_b32_e32 v64, v135
	global_load_lds_dwordx4 v[16:17], off
	s_add_i32 m0, s49, 0x2000
	v_lshl_add_u64 v[16:17], s[18:19], 0, v[64:65]
	v_lshl_add_u64 v[16:17], v[16:17], 0, s[80:81]
	s_add_u32 s18, s18, 0x20080
	global_load_lds_dwordx4 v[16:17], off
	s_addc_u32 s19, s19, 0
	v_mov_b32_e32 v16, v133
	s_add_i32 s49, s56, s22
	s_mov_b32 m0, s49
	v_mov_b32_e32 v64, v132
	global_load_lds_dwordx4 v16, s[18:19]
	v_mov_b32_e32 v16, v135
	s_add_i32 m0, s49, 0x2000
	s_nop 0
	global_load_lds_dwordx4 v16, s[18:19]
	s_mov_b32 m0, s29
	v_lshl_add_u64 v[16:17], s[16:17], 0, v[64:65]
	v_lshl_add_u64 v[16:17], v[16:17], 0, s[80:81]
	v_mov_b32_e32 v64, v134
	global_load_lds_dwordx4 v[16:17], off
	s_mov_b32 m0, s30
	v_lshl_add_u64 v[16:17], s[16:17], 0, v[64:65]
	v_lshl_add_u64 v[16:17], v[16:17], 0, s[80:81]
	global_load_lds_dwordx4 v[16:17], off
	s_waitcnt vmcnt(8)
	s_waitcnt lgkmcnt(0)
	s_barrier
	s_setprio 1
	s_waitcnt lgkmcnt(0)
	v_mfma_f32_16x16x128_f8f6f4 v[60:63], v[0:7], v[156:163], v[60:63]
	v_mfma_f32_16x16x128_f8f6f4 v[56:59], v[8:15], v[156:163], v[56:59]
	v_mfma_f32_16x16x128_f8f6f4 v[48:51], v[0:7], v[164:171], v[48:51]
	v_mfma_f32_16x16x128_f8f6f4 v[40:43], v[8:15], v[164:171], v[192:195]
	v_mfma_f32_16x16x128_f8f6f4 v[32:35], v[0:7], v[172:179], v[196:199]
	v_mfma_f32_16x16x128_f8f6f4 v[24:27], v[8:15], v[172:179], v[200:203]
	v_mfma_f32_16x16x128_f8f6f4 v[16:19], v[0:7], v[180:187], v[216:219]
	v_mfma_f32_16x16x128_f8f6f4 v[8:11], v[8:15], v[180:187], v[220:223]
	s_setprio 0
	s_setprio 1
	v_mfma_f32_16x16x128_f8f6f4 v[52:55], v[140:147], v[156:163], v[52:55]
	v_mfma_f32_16x16x128_f8f6f4 v[44:47], v[148:155], v[156:163], v[224:227]
	v_mfma_f32_16x16x128_f8f6f4 v[36:39], v[140:147], v[164:171], v[230:233]
	v_mfma_f32_16x16x128_f8f6f4 v[28:31], v[148:155], v[164:171], v[234:237]
	v_mfma_f32_16x16x128_f8f6f4 v[20:23], v[140:147], v[172:179], v[238:241]
	v_mfma_f32_16x16x128_f8f6f4 v[12:15], v[148:155], v[172:179], v[242:245]
	v_mfma_f32_16x16x128_f8f6f4 v[4:7], v[140:147], v[180:187], v[246:249]
	v_mfma_f32_16x16x128_f8f6f4 v[0:3], v[148:155], v[180:187], v[250:253]
	s_setprio 0
	s_barrier
	s_add_i32 s39, s39, 2
	s_add_u32 s14, s14, 0x100
	s_addc_u32 s15, s15, 0
	s_add_u32 s37, s37, 0x100
	s_addc_u32 s38, s38, 0
	s_cmp_gt_u32 s39, 5
	s_cbranch_scc0 .LBB0_672
	s_and_b64 vcc, exec, s[10:11]
	s_cbranch_vccz .LBB0_675
	s_barrier
.LBB0_675:
	v_mov_b32_e32 v64, v136
	v_mov_b32_e32 v130, v137
	s_mov_b32 s14, s2
	s_lshl_b32 s14, s14, 8
	s_lshl_b32 s15, s34, 8
	s_add_i32 s14, s14, s27
	s_or_b32 s15, s15, s28
	v_add_u32_e32 v140, s14, v64
	v_lshl_add_u32 v130, v130, 3, s15
	v_ashrrev_i32_e32 v141, 31, v140
	v_readlane_b32 s14, v254, 24
	v_lshlrev_b64 v[140:141], 11, v[140:141]
	v_readlane_b32 s15, v254, 25
	v_ashrrev_i32_e32 v131, 31, v130
	v_pk_mul_f32 v[128:129], v[128:129], s[58:59] op_sel_hi:[1,0]
	v_lshl_add_u64 v[140:141], s[14:15], 0, v[140:141]
	v_lshl_add_u64 v[130:131], v[130:131], 1, v[140:141]
	v_pk_mul_f32 v[126:127], v[126:127], s[58:59] op_sel_hi:[1,0]
	v_pk_mul_f32 v[140:141], v[124:125], s[58:59] op_sel_hi:[1,0]
	v_pk_mul_f32 v[124:125], v[122:123], s[58:59] op_sel_hi:[1,0]
	v_cvt_pk_bf16_f32 v122, v126, v127
	v_cvt_pk_bf16_f32 v123, v128, v129
	v_pk_mul_f32 v[120:121], v[120:121], s[58:59] op_sel_hi:[1,0]
	v_cvt_pk_bf16_f32 v124, v124, v125
	v_cvt_pk_bf16_f32 v125, v140, v141
	global_store_dwordx4 v[130:131], v[122:125], off sc1
	v_pk_mul_f32 v[118:119], v[118:119], s[58:59] op_sel_hi:[1,0]
	s_mov_b64 s[14:15], 0x8000
	v_pk_mul_f32 v[122:123], v[112:113], s[58:59] op_sel_hi:[1,0]
	v_pk_mul_f32 v[112:113], v[110:111], s[58:59] op_sel_hi:[1,0]
	v_cvt_pk_bf16_f32 v110, v118, v119
	v_cvt_pk_bf16_f32 v111, v120, v121
	v_pk_mul_f32 v[114:115], v[114:115], s[58:59] op_sel_hi:[1,0]
	v_cvt_pk_bf16_f32 v112, v112, v113
	v_cvt_pk_bf16_f32 v113, v122, v123
	global_store_dwordx4 v[130:131], v[110:113], off offset:256 sc1
	v_pk_mul_f32 v[104:105], v[104:105], s[58:59] op_sel_hi:[1,0]
	v_pk_mul_f32 v[102:103], v[102:103], s[58:59] op_sel_hi:[1,0]
	v_lshl_add_u64 v[110:111], v[130:131], 0, s[14:15]
	v_pk_mul_f32 v[112:113], v[116:117], s[58:59] op_sel_hi:[1,0]
	s_mov_b32 s14, 0x8000
	v_pk_mul_f32 v[116:117], v[108:109], s[58:59] op_sel_hi:[1,0]
	v_pk_mul_f32 v[108:109], v[106:107], s[58:59] op_sel_hi:[1,0]
	v_cvt_pk_bf16_f32 v106, v114, v115
	v_cvt_pk_bf16_f32 v107, v112, v113
	v_add_co_u32_e32 v112, vcc, s14, v130
	v_cvt_pk_bf16_f32 v108, v108, v109
	v_cvt_pk_bf16_f32 v109, v116, v117
	s_mov_b64 s[14:15], 0x10000
	s_nop 0
	v_addc_co_u32_e32 v113, vcc, 0, v131, vcc
	global_store_dwordx4 v[112:113], v[106:109], off sc1
	v_pk_mul_f32 v[98:99], v[98:99], s[58:59] op_sel_hi:[1,0]
	v_pk_mul_f32 v[88:89], v[88:89], s[58:59] op_sel_hi:[1,0]
	v_pk_mul_f32 v[106:107], v[96:97], s[58:59] op_sel_hi:[1,0]
	v_pk_mul_f32 v[96:97], v[94:95], s[58:59] op_sel_hi:[1,0]
	v_cvt_pk_bf16_f32 v94, v102, v103
	v_cvt_pk_bf16_f32 v95, v104, v105
	v_pk_mul_f32 v[86:87], v[86:87], s[58:59] op_sel_hi:[1,0]
	v_cvt_pk_bf16_f32 v96, v96, v97
	v_cvt_pk_bf16_f32 v97, v106, v107
	global_store_dwordx4 v[110:111], v[94:97], off offset:256 sc1
	v_pk_mul_f32 v[82:83], v[82:83], s[58:59] op_sel_hi:[1,0]
	v_pk_mul_f32 v[72:73], v[72:73], s[58:59] op_sel_hi:[1,0]
	v_lshl_add_u64 v[94:95], v[130:131], 0, s[14:15]
	v_pk_mul_f32 v[96:97], v[100:101], s[58:59] op_sel_hi:[1,0]
	s_mov_b32 s14, 0x10000
	v_pk_mul_f32 v[100:101], v[92:93], s[58:59] op_sel_hi:[1,0]
	v_pk_mul_f32 v[92:93], v[90:91], s[58:59] op_sel_hi:[1,0]
	v_cvt_pk_bf16_f32 v90, v98, v99
	v_cvt_pk_bf16_f32 v91, v96, v97
	v_add_co_u32_e32 v96, vcc, s14, v130
	v_cvt_pk_bf16_f32 v92, v92, v93
	v_cvt_pk_bf16_f32 v93, v100, v101
	s_mov_b64 s[14:15], 0x18000
	s_nop 0
	v_addc_co_u32_e32 v97, vcc, 0, v131, vcc
	global_store_dwordx4 v[96:97], v[90:93], off sc1
	v_pk_mul_f32 v[70:71], v[70:71], s[58:59] op_sel_hi:[1,0]
	v_pk_mul_f32 v[60:61], v[60:61], s[58:59] op_sel_hi:[1,0]
	v_pk_mul_f32 v[90:91], v[80:81], s[58:59] op_sel_hi:[1,0]
	v_pk_mul_f32 v[80:81], v[78:79], s[58:59] op_sel_hi:[1,0]
	v_cvt_pk_bf16_f32 v78, v86, v87
	v_cvt_pk_bf16_f32 v79, v88, v89
	v_pk_mul_f32 v[62:63], v[62:63], s[58:59] op_sel_hi:[1,0]
	v_cvt_pk_bf16_f32 v80, v80, v81
	v_cvt_pk_bf16_f32 v81, v90, v91
	global_store_dwordx4 v[94:95], v[78:81], off offset:256 sc1
	v_pk_mul_f32 v[54:55], v[54:55], s[58:59] op_sel_hi:[1,0]
	v_pk_mul_f32 v[52:53], v[52:53], s[58:59] op_sel_hi:[1,0]
	v_lshl_add_u64 v[78:79], v[130:131], 0, s[14:15]
	v_pk_mul_f32 v[80:81], v[84:85], s[58:59] op_sel_hi:[1,0]
	s_mov_b32 s14, 0x18000
	v_pk_mul_f32 v[84:85], v[76:77], s[58:59] op_sel_hi:[1,0]
	v_pk_mul_f32 v[76:77], v[74:75], s[58:59] op_sel_hi:[1,0]
	v_cvt_pk_bf16_f32 v74, v82, v83
	v_cvt_pk_bf16_f32 v75, v80, v81
	v_add_co_u32_e32 v80, vcc, s14, v130
	v_cvt_pk_bf16_f32 v76, v76, v77
	v_cvt_pk_bf16_f32 v77, v84, v85
	s_mov_b32 s14, 0x40000
	s_nop 0
	v_addc_co_u32_e32 v81, vcc, 0, v131, vcc
	global_store_dwordx4 v[80:81], v[74:77], off sc1
	v_pk_mul_f32 v[48:49], v[48:49], s[58:59] op_sel_hi:[1,0]
	v_pk_mul_f32 v[38:39], v[38:39], s[58:59] op_sel_hi:[1,0]
	v_pk_mul_f32 v[74:75], v[68:69], s[58:59] op_sel_hi:[1,0]
	v_pk_mul_f32 v[68:69], v[66:67], s[58:59] op_sel_hi:[1,0]
	v_cvt_pk_bf16_f32 v66, v70, v71
	v_cvt_pk_bf16_f32 v67, v72, v73
	v_pk_mul_f32 v[36:37], v[36:37], s[58:59] op_sel_hi:[1,0]
	v_cvt_pk_bf16_f32 v68, v68, v69
	v_cvt_pk_bf16_f32 v69, v74, v75
	global_store_dwordx4 v[78:79], v[66:69], off offset:256 sc1
	v_pk_mul_f32 v[32:33], v[32:33], s[58:59] op_sel_hi:[1,0]
	v_pk_mul_f32 v[22:23], v[22:23], s[58:59] op_sel_hi:[1,0]
	v_pk_mul_f32 v[68:69], v[58:59], s[58:59] op_sel_hi:[1,0]
	v_pk_mul_f32 v[58:59], v[56:57], s[58:59] op_sel_hi:[1,0]
	v_cvt_pk_bf16_f32 v56, v60, v61
	v_add_co_u32_e32 v60, vcc, s14, v130
	v_cvt_pk_bf16_f32 v57, v62, v63
	v_cvt_pk_bf16_f32 v58, v58, v59
	v_cvt_pk_bf16_f32 v59, v68, v69
	v_lshl_add_u64 v[66:67], v[130:131], 0, s[90:91]
	s_nop 0
	v_addc_co_u32_e32 v61, vcc, 0, v131, vcc
	global_store_dwordx4 v[60:61], v[56:59], off sc1
	s_mov_b64 s[14:15], 0x48000
	v_pk_mul_f32 v[20:21], v[20:21], s[58:59] op_sel_hi:[1,0]
	v_pk_mul_f32 v[56:57], v[46:47], s[58:59] op_sel_hi:[1,0]
	v_pk_mul_f32 v[46:47], v[44:45], s[58:59] op_sel_hi:[1,0]
	v_cvt_pk_bf16_f32 v44, v52, v53
	v_cvt_pk_bf16_f32 v45, v54, v55
	v_pk_mul_f32 v[16:17], v[16:17], s[58:59] op_sel_hi:[1,0]
	v_cvt_pk_bf16_f32 v46, v46, v47
	v_cvt_pk_bf16_f32 v47, v56, v57
	global_store_dwordx4 v[66:67], v[44:47], off offset:256 sc1
	s_cmp_eq_u32 s34, 3
	v_pk_mul_f32 v[6:7], v[6:7], s[58:59] op_sel_hi:[1,0]
	v_lshl_add_u64 v[44:45], v[130:131], 0, s[14:15]
	v_pk_mul_f32 v[46:47], v[50:51], s[58:59] op_sel_hi:[1,0]
	s_mov_b32 s14, 0x48000
	v_pk_mul_f32 v[50:51], v[42:43], s[58:59] op_sel_hi:[1,0]
	v_pk_mul_f32 v[42:43], v[40:41], s[58:59] op_sel_hi:[1,0]
	v_cvt_pk_bf16_f32 v40, v48, v49
	v_cvt_pk_bf16_f32 v41, v46, v47
	v_add_co_u32_e32 v46, vcc, s14, v130
	v_cvt_pk_bf16_f32 v42, v42, v43
	v_cvt_pk_bf16_f32 v43, v50, v51
	s_mov_b64 s[14:15], 0x50000
	s_nop 0
	v_addc_co_u32_e32 v47, vcc, 0, v131, vcc
	global_store_dwordx4 v[46:47], v[40:43], off sc1
	v_pk_mul_f32 v[4:5], v[4:5], s[58:59] op_sel_hi:[1,0]
	s_nop 0
	v_pk_mul_f32 v[40:41], v[30:31], s[58:59] op_sel_hi:[1,0]
	v_pk_mul_f32 v[30:31], v[28:29], s[58:59] op_sel_hi:[1,0]
	v_cvt_pk_bf16_f32 v28, v36, v37
	v_cvt_pk_bf16_f32 v29, v38, v39
	s_nop 0
	v_cvt_pk_bf16_f32 v30, v30, v31
	v_cvt_pk_bf16_f32 v31, v40, v41
	global_store_dwordx4 v[44:45], v[28:31], off offset:256 sc1
	s_nop 1
	v_lshl_add_u64 v[28:29], v[130:131], 0, s[14:15]
	v_pk_mul_f32 v[30:31], v[34:35], s[58:59] op_sel_hi:[1,0]
	s_mov_b32 s14, 0x50000
	v_pk_mul_f32 v[34:35], v[26:27], s[58:59] op_sel_hi:[1,0]
	v_pk_mul_f32 v[26:27], v[24:25], s[58:59] op_sel_hi:[1,0]
	v_cvt_pk_bf16_f32 v24, v32, v33
	v_cvt_pk_bf16_f32 v25, v30, v31
	v_add_co_u32_e32 v30, vcc, s14, v130
	v_cvt_pk_bf16_f32 v26, v26, v27
	v_cvt_pk_bf16_f32 v27, v34, v35
	s_mov_b64 s[14:15], 0x58000
	s_nop 0
	v_addc_co_u32_e32 v31, vcc, 0, v131, vcc
	global_store_dwordx4 v[30:31], v[24:27], off sc1
	s_nop 1
	v_pk_mul_f32 v[24:25], v[14:15], s[58:59] op_sel_hi:[1,0]
	v_pk_mul_f32 v[14:15], v[12:13], s[58:59] op_sel_hi:[1,0]
	v_cvt_pk_bf16_f32 v12, v20, v21
	v_cvt_pk_bf16_f32 v13, v22, v23
	s_nop 0
	v_cvt_pk_bf16_f32 v14, v14, v15
	v_cvt_pk_bf16_f32 v15, v24, v25
	global_store_dwordx4 v[28:29], v[12:15], off offset:256 sc1
	s_nop 1
	v_lshl_add_u64 v[12:13], v[130:131], 0, s[14:15]
	v_pk_mul_f32 v[14:15], v[18:19], s[58:59] op_sel_hi:[1,0]
	s_mov_b32 s14, 0x58000
	v_pk_mul_f32 v[18:19], v[10:11], s[58:59] op_sel_hi:[1,0]
	v_pk_mul_f32 v[10:11], v[8:9], s[58:59] op_sel_hi:[1,0]
	v_cvt_pk_bf16_f32 v8, v16, v17
	v_cvt_pk_bf16_f32 v9, v14, v15
	v_add_co_u32_e32 v14, vcc, s14, v130
	v_cvt_pk_bf16_f32 v10, v10, v11
	v_cvt_pk_bf16_f32 v11, v18, v19
	s_mov_b64 s[14:15], -1
	s_nop 0
	v_addc_co_u32_e32 v15, vcc, 0, v131, vcc
	global_store_dwordx4 v[14:15], v[8:11], off sc1
	s_nop 1
	v_pk_mul_f32 v[8:9], v[2:3], s[58:59] op_sel_hi:[1,0]
	v_pk_mul_f32 v[2:3], v[0:1], s[58:59] op_sel_hi:[1,0]
	v_cvt_pk_bf16_f32 v0, v4, v5
	v_cvt_pk_bf16_f32 v1, v6, v7
	s_nop 0
	v_cvt_pk_bf16_f32 v2, v2, v3
	v_cvt_pk_bf16_f32 v3, v8, v9
	global_store_dwordx4 v[12:13], v[0:3], off offset:256 sc1
	s_mov_b32 s99, 1
	s_cbranch_scc1 .LBB0_670
	s_andn2_b64 vcc, exec, s[8:9]
	s_cbranch_vccnz .LBB0_669
	s_barrier
	s_branch .LBB0_669

.LBB0_686:
	s_add_u32 s16, s14, 0xfffc0080
	s_addc_u32 s17, s15, -1
	s_add_i32 s38, 0, 0x10000
	s_cmp_eq_u32 s37, 12
	s_cselect_b32 s17, s93, s17
	s_cselect_b32 s16, s92, s16
	v_add_u32_e32 v64, s38, v138
	s_cselect_b32 s19, s31, s36
	s_cselect_b32 s18, s34, s35
	s_add_i32 s49, 0, 0x14000
	ds_read_b128 v[140:143], v64
	ds_read_b128 v[144:147], v64 offset:1024
	ds_read_b128 v[148:151], v64 offset:2048
	ds_read_b128 v[152:155], v64 offset:3072
	v_add_u32_e32 v64, s49, v138
	ds_read_b128 v[156:159], v64
	ds_read_b128 v[160:163], v64 offset:1024
	ds_read_b128 v[164:167], v64 offset:2048
	ds_read_b128 v[168:171], v64 offset:3072
	v_mov_b32_e32 v64, v132
	ds_read_b128 v[172:175], v139
	ds_read_b128 v[176:179], v139 offset:1024
	ds_read_b128 v[180:183], v139 offset:2048
	ds_read_b128 v[184:187], v139 offset:3072
	ds_read_b128 v[188:191], v139 offset:4096
	ds_read_b128 v[192:195], v139 offset:5120
	ds_read_b128 v[196:199], v139 offset:6144
	ds_read_b128 v[200:203], v139 offset:7168
	s_add_i32 m0, s21, 0xc000
	s_nop 0
	global_load_lds_dwordx4 v64, s[14:15]
	v_mov_b32_e32 v64, v134
	s_add_i32 m0, s21, 0xe000
	s_nop 0
	global_load_lds_dwordx4 v64, s[14:15]
	s_cmp_eq_u32 s99, 0
	s_cbranch_scc1 .Lrw_ob1_n
	s_waitcnt vmcnt(24)
	s_branch .Lrw_ob1_d

.Lrw_ob1_d:
	s_waitcnt lgkmcnt(0)
	s_barrier
	s_setprio 1
	s_waitcnt lgkmcnt(0)
	v_mfma_f32_16x16x32_bf16 v[126:129], v[140:143], v[172:175], v[126:129]
	v_mfma_f32_16x16x32_bf16 v[122:125], v[148:151], v[172:175], v[122:125]
	v_mfma_f32_16x16x32_bf16 v[118:121], v[140:143], v[180:183], v[118:121]
	v_mfma_f32_16x16x32_bf16 v[110:113], v[148:151], v[180:183], v[110:113]
	v_mfma_f32_16x16x32_bf16 v[102:105], v[140:143], v[188:191], v[102:105]
	v_mfma_f32_16x16x32_bf16 v[94:97], v[148:151], v[188:191], v[94:97]
	v_mfma_f32_16x16x32_bf16 v[86:89], v[140:143], v[196:199], v[86:89]
	v_mfma_f32_16x16x32_bf16 v[78:81], v[148:151], v[196:199], v[78:81]
	v_mfma_f32_16x16x32_bf16 v[126:129], v[144:147], v[176:179], v[126:129]
	v_mfma_f32_16x16x32_bf16 v[122:125], v[152:155], v[176:179], v[122:125]
	v_mfma_f32_16x16x32_bf16 v[118:121], v[144:147], v[184:187], v[118:121]
	v_mfma_f32_16x16x32_bf16 v[110:113], v[152:155], v[184:187], v[110:113]
	v_mfma_f32_16x16x32_bf16 v[102:105], v[144:147], v[192:195], v[102:105]
	v_mfma_f32_16x16x32_bf16 v[94:97], v[152:155], v[192:195], v[94:97]
	v_mfma_f32_16x16x32_bf16 v[86:89], v[144:147], v[200:203], v[86:89]
	v_mfma_f32_16x16x32_bf16 v[78:81], v[152:155], v[200:203], v[78:81]
	s_setprio 0
	s_setprio 1
	v_mfma_f32_16x16x32_bf16 v[114:117], v[156:159], v[172:175], v[114:117]
	v_mfma_f32_16x16x32_bf16 v[106:109], v[164:167], v[172:175], v[106:109]
	v_mfma_f32_16x16x32_bf16 v[98:101], v[156:159], v[180:183], v[98:101]
	v_mfma_f32_16x16x32_bf16 v[90:93], v[164:167], v[180:183], v[90:93]
	v_mfma_f32_16x16x32_bf16 v[82:85], v[156:159], v[188:191], v[82:85]
	v_mfma_f32_16x16x32_bf16 v[74:77], v[164:167], v[188:191], v[74:77]
	v_mfma_f32_16x16x32_bf16 v[70:73], v[156:159], v[196:199], v[70:73]
	v_mfma_f32_16x16x32_bf16 v[66:69], v[164:167], v[196:199], v[66:69]
	v_mfma_f32_16x16x32_bf16 v[114:117], v[160:163], v[176:179], v[114:117]
	v_mfma_f32_16x16x32_bf16 v[106:109], v[168:171], v[176:179], v[106:109]
	v_mfma_f32_16x16x32_bf16 v[98:101], v[160:163], v[184:187], v[98:101]
	v_mfma_f32_16x16x32_bf16 v[90:93], v[168:171], v[184:187], v[90:93]
	v_mfma_f32_16x16x32_bf16 v[82:85], v[160:163], v[192:195], v[82:85]
	v_mfma_f32_16x16x32_bf16 v[74:77], v[168:171], v[192:195], v[74:77]
	v_mfma_f32_16x16x32_bf16 v[70:73], v[160:163], v[200:203], v[70:73]
	v_mfma_f32_16x16x32_bf16 v[66:69], v[168:171], v[200:203], v[66:69]
	s_setprio 0
	s_barrier
	v_mov_b32_e32 v64, v133
	s_add_i32 s38, s38, s20
	ds_read_b128 v[172:175], v139 offset:16384
	ds_read_b128 v[176:179], v139 offset:17408
	ds_read_b128 v[180:183], v139 offset:18432
	ds_read_b128 v[184:187], v139 offset:19456
	ds_read_b128 v[188:191], v139 offset:20480
	ds_read_b128 v[192:195], v139 offset:21504
	ds_read_b128 v[196:199], v139 offset:22528
	ds_read_b128 v[200:203], v139 offset:23552
	s_mov_b32 m0, s38
	s_nop 0
	global_load_lds_dwordx4 v64, s[18:19]
	v_mov_b32_e32 v64, v135
	s_add_i32 m0, s38, 0x2000
	s_add_u32 s38, s18, 0x40000
	global_load_lds_dwordx4 v64, s[18:19]
	s_addc_u32 s39, s19, 0
	v_mov_b32_e32 v64, v133
	s_add_i32 s49, s49, s20
	s_mov_b32 m0, s49
	s_nop 0
	global_load_lds_dwordx4 v64, s[38:39]
	v_mov_b32_e32 v64, v135
	s_add_i32 m0, s49, 0x2000
	s_nop 0
	global_load_lds_dwordx4 v64, s[38:39]
	v_mov_b32_e32 v64, v132
	s_mov_b32 m0, s21
	s_nop 0
	global_load_lds_dwordx4 v64, s[16:17]
	v_mov_b32_e32 v64, v134
	s_mov_b32 m0, s22
	s_nop 0
	global_load_lds_dwordx4 v64, s[16:17]
	s_cmp_eq_u32 s99, 0
	s_cbranch_scc1 .Lrw_ob2_n
	s_waitcnt vmcnt(24)
	s_branch .Lrw_ob2_d

.Lrw_ob2_d:
	s_mov_b32 s99, 0
	s_waitcnt lgkmcnt(0)
	s_barrier
	s_setprio 1
	s_waitcnt lgkmcnt(0)
	v_mfma_f32_16x16x32_bf16 v[60:63], v[140:143], v[172:175], v[60:63]
	v_mfma_f32_16x16x32_bf16 v[56:59], v[148:151], v[172:175], v[56:59]
	v_mfma_f32_16x16x32_bf16 v[52:55], v[140:143], v[180:183], v[52:55]
	v_mfma_f32_16x16x32_bf16 v[44:47], v[148:151], v[180:183], v[44:47]
	v_mfma_f32_16x16x32_bf16 v[36:39], v[140:143], v[188:191], v[36:39]
	v_mfma_f32_16x16x32_bf16 v[28:31], v[148:151], v[188:191], v[28:31]
	v_mfma_f32_16x16x32_bf16 v[20:23], v[140:143], v[196:199], v[20:23]
	v_mfma_f32_16x16x32_bf16 v[12:15], v[148:151], v[196:199], v[12:15]
	v_mfma_f32_16x16x32_bf16 v[60:63], v[144:147], v[176:179], v[60:63]
	v_mfma_f32_16x16x32_bf16 v[56:59], v[152:155], v[176:179], v[56:59]
	v_mfma_f32_16x16x32_bf16 v[52:55], v[144:147], v[184:187], v[52:55]
	v_mfma_f32_16x16x32_bf16 v[44:47], v[152:155], v[184:187], v[44:47]
	v_mfma_f32_16x16x32_bf16 v[36:39], v[144:147], v[192:195], v[36:39]
	v_mfma_f32_16x16x32_bf16 v[28:31], v[152:155], v[192:195], v[28:31]
	v_mfma_f32_16x16x32_bf16 v[20:23], v[144:147], v[200:203], v[20:23]
	v_mfma_f32_16x16x32_bf16 v[12:15], v[152:155], v[200:203], v[12:15]
	s_setprio 0
	s_setprio 1
	v_mfma_f32_16x16x32_bf16 v[48:51], v[156:159], v[172:175], v[48:51]
	v_mfma_f32_16x16x32_bf16 v[40:43], v[164:167], v[172:175], v[40:43]
	v_mfma_f32_16x16x32_bf16 v[32:35], v[156:159], v[180:183], v[32:35]
	v_mfma_f32_16x16x32_bf16 v[24:27], v[164:167], v[180:183], v[24:27]
	v_mfma_f32_16x16x32_bf16 v[16:19], v[156:159], v[188:191], v[16:19]
	v_mfma_f32_16x16x32_bf16 v[8:11], v[164:167], v[188:191], v[8:11]
	v_mfma_f32_16x16x32_bf16 v[4:7], v[156:159], v[196:199], v[4:7]
	v_mfma_f32_16x16x32_bf16 v[0:3], v[164:167], v[196:199], v[0:3]
	v_mfma_f32_16x16x32_bf16 v[48:51], v[160:163], v[176:179], v[48:51]
	v_mfma_f32_16x16x32_bf16 v[40:43], v[168:171], v[176:179], v[40:43]
	v_mfma_f32_16x16x32_bf16 v[32:35], v[160:163], v[184:187], v[32:35]
	v_mfma_f32_16x16x32_bf16 v[24:27], v[168:171], v[184:187], v[24:27]
	v_mfma_f32_16x16x32_bf16 v[16:19], v[160:163], v[192:195], v[16:19]
	v_mfma_f32_16x16x32_bf16 v[8:11], v[168:171], v[192:195], v[8:11]
	v_mfma_f32_16x16x32_bf16 v[4:7], v[160:163], v[200:203], v[4:7]
	v_mfma_f32_16x16x32_bf16 v[0:3], v[168:171], v[200:203], v[0:3]
	s_setprio 0
	s_barrier
	s_add_i32 s49, 0, 0x18000
	v_add_u32_e32 v64, s49, v138
	s_add_i32 s50, 0, 0x1c000
	ds_read_b128 v[140:143], v64
	ds_read_b128 v[144:147], v64 offset:1024
	ds_read_b128 v[148:151], v64 offset:2048
	ds_read_b128 v[152:155], v64 offset:3072
	v_add_u32_e32 v64, s50, v138
	ds_read_b128 v[156:159], v64
	ds_read_b128 v[160:163], v64 offset:1024
	ds_read_b128 v[164:167], v64 offset:2048
	ds_read_b128 v[168:171], v64 offset:3072
	s_add_u32 s38, s16, 0x40000
	v_mov_b32_e32 v64, v132
	s_mov_b32 m0, s23
	ds_read_b128 v[172:175], v139 offset:32768
	ds_read_b128 v[176:179], v139 offset:33792
	ds_read_b128 v[180:183], v139 offset:34816
	ds_read_b128 v[184:187], v139 offset:35840
	ds_read_b128 v[188:191], v139 offset:36864
	ds_read_b128 v[192:195], v139 offset:37888
	ds_read_b128 v[196:199], v139 offset:38912
	ds_read_b128 v[200:203], v139 offset:39936
	s_addc_u32 s39, s17, 0
	s_nop 0
	global_load_lds_dwordx4 v64, s[38:39]
	v_mov_b32_e32 v64, v134
	s_mov_b32 m0, s24
	s_nop 0
	global_load_lds_dwordx4 v64, s[38:39]
	s_waitcnt vmcnt(8)
	s_waitcnt lgkmcnt(0)
	s_barrier
	s_setprio 1
	s_waitcnt lgkmcnt(0)
	v_mfma_f32_16x16x32_bf16 v[126:129], v[140:143], v[172:175], v[126:129]
	v_mfma_f32_16x16x32_bf16 v[122:125], v[148:151], v[172:175], v[122:125]
	v_mfma_f32_16x16x32_bf16 v[118:121], v[140:143], v[180:183], v[118:121]
	v_mfma_f32_16x16x32_bf16 v[110:113], v[148:151], v[180:183], v[110:113]
	v_mfma_f32_16x16x32_bf16 v[102:105], v[140:143], v[188:191], v[102:105]
	v_mfma_f32_16x16x32_bf16 v[94:97], v[148:151], v[188:191], v[94:97]
	v_mfma_f32_16x16x32_bf16 v[86:89], v[140:143], v[196:199], v[86:89]
	v_mfma_f32_16x16x32_bf16 v[78:81], v[148:151], v[196:199], v[78:81]
	v_mfma_f32_16x16x32_bf16 v[126:129], v[144:147], v[176:179], v[126:129]
	v_mfma_f32_16x16x32_bf16 v[122:125], v[152:155], v[176:179], v[122:125]
	v_mfma_f32_16x16x32_bf16 v[118:121], v[144:147], v[184:187], v[118:121]
	v_mfma_f32_16x16x32_bf16 v[110:113], v[152:155], v[184:187], v[110:113]
	v_mfma_f32_16x16x32_bf16 v[102:105], v[144:147], v[192:195], v[102:105]
	v_mfma_f32_16x16x32_bf16 v[94:97], v[152:155], v[192:195], v[94:97]
	v_mfma_f32_16x16x32_bf16 v[86:89], v[144:147], v[200:203], v[86:89]
	v_mfma_f32_16x16x32_bf16 v[78:81], v[152:155], v[200:203], v[78:81]
	s_setprio 0
	s_setprio 1
	v_mfma_f32_16x16x32_bf16 v[114:117], v[156:159], v[172:175], v[114:117]
	v_mfma_f32_16x16x32_bf16 v[106:109], v[164:167], v[172:175], v[106:109]
	v_mfma_f32_16x16x32_bf16 v[98:101], v[156:159], v[180:183], v[98:101]
	v_mfma_f32_16x16x32_bf16 v[90:93], v[164:167], v[180:183], v[90:93]
	v_mfma_f32_16x16x32_bf16 v[82:85], v[156:159], v[188:191], v[82:85]
	v_mfma_f32_16x16x32_bf16 v[74:77], v[164:167], v[188:191], v[74:77]
	v_mfma_f32_16x16x32_bf16 v[70:73], v[156:159], v[196:199], v[70:73]
	v_mfma_f32_16x16x32_bf16 v[66:69], v[164:167], v[196:199], v[66:69]
	v_mfma_f32_16x16x32_bf16 v[114:117], v[160:163], v[176:179], v[114:117]
	v_mfma_f32_16x16x32_bf16 v[106:109], v[168:171], v[176:179], v[106:109]
	v_mfma_f32_16x16x32_bf16 v[98:101], v[160:163], v[184:187], v[98:101]
	v_mfma_f32_16x16x32_bf16 v[90:93], v[168:171], v[184:187], v[90:93]
	v_mfma_f32_16x16x32_bf16 v[82:85], v[160:163], v[192:195], v[82:85]
	v_mfma_f32_16x16x32_bf16 v[74:77], v[168:171], v[192:195], v[74:77]
	v_mfma_f32_16x16x32_bf16 v[70:73], v[160:163], v[200:203], v[70:73]
	v_mfma_f32_16x16x32_bf16 v[66:69], v[168:171], v[200:203], v[66:69]
	s_setprio 0
	s_barrier
	v_mov_b32_e32 v64, v133
	ds_read_b128 v[172:175], v139 offset:49152
	ds_read_b128 v[176:179], v139 offset:50176
	ds_read_b128 v[180:183], v139 offset:51200
	ds_read_b128 v[184:187], v139 offset:52224
	ds_read_b128 v[188:191], v139 offset:53248
	ds_read_b128 v[192:195], v139 offset:54272
	ds_read_b128 v[196:199], v139 offset:55296
	ds_read_b128 v[200:203], v139 offset:56320
	s_add_i32 s38, s49, s20
	v_lshl_add_u64 v[130:131], s[18:19], 0, v[64:65]
	v_lshl_add_u64 v[130:131], v[130:131], 0, s[80:81]
	s_mov_b32 m0, s38
	v_mov_b32_e32 v64, v135
	global_load_lds_dwordx4 v[130:131], off
	s_add_i32 m0, s38, 0x2000
	s_nop 0
	v_lshl_add_u64 v[130:131], s[18:19], 0, v[64:65]
	s_add_u32 s18, s18, 0x40080
	v_lshl_add_u64 v[130:131], v[130:131], 0, s[80:81]
	s_addc_u32 s19, s19, 0
	v_mov_b32_e32 v64, v133
	s_add_i32 s38, s50, s20
	global_load_lds_dwordx4 v[130:131], off
	s_mov_b32 m0, s38
	s_nop 0
	global_load_lds_dwordx4 v64, s[18:19]
	v_mov_b32_e32 v64, v135
	s_add_i32 m0, s38, 0x2000
	s_nop 0
	global_load_lds_dwordx4 v64, s[18:19]
	v_mov_b32_e32 v64, v132
	s_mov_b32 m0, s27
	v_lshl_add_u64 v[130:131], s[16:17], 0, v[64:65]
	v_lshl_add_u64 v[130:131], v[130:131], 0, s[80:81]
	v_mov_b32_e32 v64, v134
	global_load_lds_dwordx4 v[130:131], off
	s_mov_b32 m0, s28
	v_lshl_add_u64 v[130:131], s[16:17], 0, v[64:65]
	v_lshl_add_u64 v[130:131], v[130:131], 0, s[80:81]
	global_load_lds_dwordx4 v[130:131], off
	s_waitcnt vmcnt(8)
	s_waitcnt lgkmcnt(0)
	s_barrier
	s_setprio 1
	s_waitcnt lgkmcnt(0)
	v_mfma_f32_16x16x32_bf16 v[60:63], v[140:143], v[172:175], v[60:63]
	v_mfma_f32_16x16x32_bf16 v[56:59], v[148:151], v[172:175], v[56:59]
	v_mfma_f32_16x16x32_bf16 v[52:55], v[140:143], v[180:183], v[52:55]
	v_mfma_f32_16x16x32_bf16 v[44:47], v[148:151], v[180:183], v[44:47]
	v_mfma_f32_16x16x32_bf16 v[36:39], v[140:143], v[188:191], v[36:39]
	v_mfma_f32_16x16x32_bf16 v[28:31], v[148:151], v[188:191], v[28:31]
	v_mfma_f32_16x16x32_bf16 v[20:23], v[140:143], v[196:199], v[20:23]
	v_mfma_f32_16x16x32_bf16 v[12:15], v[148:151], v[196:199], v[12:15]
	v_mfma_f32_16x16x32_bf16 v[60:63], v[144:147], v[176:179], v[60:63]
	v_mfma_f32_16x16x32_bf16 v[56:59], v[152:155], v[176:179], v[56:59]
	v_mfma_f32_16x16x32_bf16 v[52:55], v[144:147], v[184:187], v[52:55]
	v_mfma_f32_16x16x32_bf16 v[44:47], v[152:155], v[184:187], v[44:47]
	v_mfma_f32_16x16x32_bf16 v[36:39], v[144:147], v[192:195], v[36:39]
	v_mfma_f32_16x16x32_bf16 v[28:31], v[152:155], v[192:195], v[28:31]
	v_mfma_f32_16x16x32_bf16 v[20:23], v[144:147], v[200:203], v[20:23]
	v_mfma_f32_16x16x32_bf16 v[12:15], v[152:155], v[200:203], v[12:15]
	s_setprio 0
	s_setprio 1
	v_mfma_f32_16x16x32_bf16 v[48:51], v[156:159], v[172:175], v[48:51]
	v_mfma_f32_16x16x32_bf16 v[40:43], v[164:167], v[172:175], v[40:43]
	v_mfma_f32_16x16x32_bf16 v[32:35], v[156:159], v[180:183], v[32:35]
	v_mfma_f32_16x16x32_bf16 v[24:27], v[164:167], v[180:183], v[24:27]
	v_mfma_f32_16x16x32_bf16 v[16:19], v[156:159], v[188:191], v[16:19]
	v_mfma_f32_16x16x32_bf16 v[8:11], v[164:167], v[188:191], v[8:11]
	v_mfma_f32_16x16x32_bf16 v[4:7], v[156:159], v[196:199], v[4:7]
	v_mfma_f32_16x16x32_bf16 v[0:3], v[164:167], v[196:199], v[0:3]
	v_mfma_f32_16x16x32_bf16 v[48:51], v[160:163], v[176:179], v[48:51]
	v_mfma_f32_16x16x32_bf16 v[40:43], v[168:171], v[176:179], v[40:43]
	v_mfma_f32_16x16x32_bf16 v[32:35], v[160:163], v[184:187], v[32:35]
	v_mfma_f32_16x16x32_bf16 v[24:27], v[168:171], v[184:187], v[24:27]
	v_mfma_f32_16x16x32_bf16 v[16:19], v[160:163], v[192:195], v[16:19]
	v_mfma_f32_16x16x32_bf16 v[8:11], v[168:171], v[192:195], v[8:11]
	v_mfma_f32_16x16x32_bf16 v[4:7], v[160:163], v[200:203], v[4:7]
	v_mfma_f32_16x16x32_bf16 v[0:3], v[168:171], v[200:203], v[0:3]
	s_setprio 0
	s_barrier
	s_add_i32 s37, s37, 2
	s_add_u32 s14, s14, 0x100
	s_addc_u32 s15, s15, 0
	s_add_u32 s35, s35, 0x100
	s_addc_u32 s36, s36, 0
	s_cmp_gt_u32 s37, 13
	s_cbranch_scc0 .LBB0_686
	s_and_b64 vcc, exec, s[10:11]
	s_cbranch_vccz .LBB0_689
	s_barrier
.LBB0_689:
	v_mov_b32_e32 v64, v136
	v_mov_b32_e32 v130, v137
	s_mov_b32 s14, s2
	s_lshl_b32 s14, s14, 8
	s_lshl_b32 s15, s30, 8
	s_add_i32 s14, s14, s25
	s_or_b32 s15, s15, s26
	v_add_u32_e32 v140, s14, v64
	v_lshl_add_u32 v130, v130, 3, s15
	v_ashrrev_i32_e32 v141, 31, v140
	v_readlane_b32 s14, v254, 24
	v_lshlrev_b64 v[140:141], 11, v[140:141]
	v_readlane_b32 s15, v254, 25
	v_ashrrev_i32_e32 v131, 31, v130
	v_cvt_pk_bf16_f32 v126, v126, v127
	v_cvt_pk_bf16_f32 v127, v128, v129
	v_cvt_pk_bf16_f32 v128, v122, v123
	v_cvt_pk_bf16_f32 v129, v124, v125
	s_nop 0
	v_lshl_add_u64 v[140:141], s[14:15], 0, v[140:141]
	v_lshl_add_u64 v[130:131], v[130:131], 1, v[140:141]
	global_store_dwordx4 v[130:131], v[126:129], off sc1
	v_cvt_pk_bf16_f32 v114, v114, v115
	v_cvt_pk_bf16_f32 v115, v116, v117
	s_mov_b64 s[14:15], 0x8000
	v_cvt_pk_bf16_f32 v116, v106, v107
	v_cvt_pk_bf16_f32 v117, v108, v109
	global_store_dwordx4 v[130:131], v[114:117], off offset:256 sc1
	v_cvt_pk_bf16_f32 v106, v118, v119
	v_cvt_pk_bf16_f32 v107, v120, v121
	v_cvt_pk_bf16_f32 v108, v110, v111
	v_cvt_pk_bf16_f32 v109, v112, v113
	s_cmp_eq_u32 s30, 3
	s_nop 0
	v_lshl_add_u64 v[114:115], v[130:131], 0, s[14:15]
	s_mov_b32 s14, 0x8000
	v_add_co_u32_e32 v110, vcc, s14, v130
	s_mov_b64 s[14:15], 0x10000
	s_nop 0
	v_addc_co_u32_e32 v111, vcc, 0, v131, vcc
	global_store_dwordx4 v[110:111], v[106:109], off sc1
	v_cvt_pk_bf16_f32 v98, v98, v99
	v_cvt_pk_bf16_f32 v99, v100, v101
	v_cvt_pk_bf16_f32 v100, v90, v91
	v_cvt_pk_bf16_f32 v101, v92, v93
	global_store_dwordx4 v[114:115], v[98:101], off offset:256 sc1
	v_cvt_pk_bf16_f32 v90, v102, v103
	v_cvt_pk_bf16_f32 v91, v104, v105
	v_cvt_pk_bf16_f32 v92, v94, v95
	v_cvt_pk_bf16_f32 v93, v96, v97
	s_nop 1
	v_lshl_add_u64 v[98:99], v[130:131], 0, s[14:15]
	s_mov_b32 s14, 0x10000
	v_add_co_u32_e32 v94, vcc, s14, v130
	s_mov_b64 s[14:15], 0x18000
	s_nop 0
	v_addc_co_u32_e32 v95, vcc, 0, v131, vcc
	global_store_dwordx4 v[94:95], v[90:93], off sc1
	v_cvt_pk_bf16_f32 v82, v82, v83
	v_cvt_pk_bf16_f32 v83, v84, v85
	v_cvt_pk_bf16_f32 v84, v74, v75
	v_cvt_pk_bf16_f32 v85, v76, v77
	global_store_dwordx4 v[98:99], v[82:85], off offset:256 sc1
	v_cvt_pk_bf16_f32 v74, v86, v87
	v_cvt_pk_bf16_f32 v75, v88, v89
	v_cvt_pk_bf16_f32 v76, v78, v79
	v_cvt_pk_bf16_f32 v77, v80, v81
	s_nop 1
	v_lshl_add_u64 v[82:83], v[130:131], 0, s[14:15]
	s_mov_b32 s14, 0x18000
	v_add_co_u32_e32 v78, vcc, s14, v130
	s_mov_b32 s14, 0x40000
	s_nop 0
	v_addc_co_u32_e32 v79, vcc, 0, v131, vcc
	global_store_dwordx4 v[78:79], v[74:77], off sc1
	v_cvt_pk_bf16_f32 v70, v70, v71
	v_cvt_pk_bf16_f32 v71, v72, v73
	v_cvt_pk_bf16_f32 v72, v66, v67
	v_cvt_pk_bf16_f32 v73, v68, v69
	global_store_dwordx4 v[82:83], v[70:73], off offset:256 sc1
	v_cvt_pk_bf16_f32 v60, v60, v61
	v_cvt_pk_bf16_f32 v61, v62, v63
	v_cvt_pk_bf16_f32 v62, v56, v57
	v_add_co_u32_e32 v56, vcc, s14, v130
	v_lshl_add_u64 v[66:67], v[130:131], 0, s[90:91]
	s_nop 0
	v_addc_co_u32_e32 v57, vcc, 0, v131, vcc
	v_cvt_pk_bf16_f32 v63, v58, v59
	global_store_dwordx4 v[56:57], v[60:63], off sc1
	v_cvt_pk_bf16_f32 v48, v48, v49
	v_cvt_pk_bf16_f32 v49, v50, v51
	s_mov_b64 s[14:15], 0x48000
	v_cvt_pk_bf16_f32 v50, v40, v41
	v_cvt_pk_bf16_f32 v51, v42, v43
	global_store_dwordx4 v[66:67], v[48:51], off offset:256 sc1
	v_cvt_pk_bf16_f32 v40, v52, v53
	v_cvt_pk_bf16_f32 v41, v54, v55
	v_cvt_pk_bf16_f32 v42, v44, v45
	v_cvt_pk_bf16_f32 v43, v46, v47
	s_nop 1
	v_lshl_add_u64 v[48:49], v[130:131], 0, s[14:15]
	s_mov_b32 s14, 0x48000
	v_add_co_u32_e32 v44, vcc, s14, v130
	s_mov_b64 s[14:15], 0x50000
	s_nop 0
	v_addc_co_u32_e32 v45, vcc, 0, v131, vcc
	global_store_dwordx4 v[44:45], v[40:43], off sc1
	v_cvt_pk_bf16_f32 v32, v32, v33
	v_cvt_pk_bf16_f32 v33, v34, v35
	v_cvt_pk_bf16_f32 v34, v24, v25
	v_cvt_pk_bf16_f32 v35, v26, v27
	global_store_dwordx4 v[48:49], v[32:35], off offset:256 sc1
	v_cvt_pk_bf16_f32 v24, v36, v37
	v_cvt_pk_bf16_f32 v25, v38, v39
	v_cvt_pk_bf16_f32 v26, v28, v29
	v_cvt_pk_bf16_f32 v27, v30, v31
	s_nop 1
	v_lshl_add_u64 v[32:33], v[130:131], 0, s[14:15]
	s_mov_b32 s14, 0x50000
	v_add_co_u32_e32 v28, vcc, s14, v130
	s_mov_b64 s[14:15], 0x58000
	s_nop 0
	v_addc_co_u32_e32 v29, vcc, 0, v131, vcc
	global_store_dwordx4 v[28:29], v[24:27], off sc1
	v_cvt_pk_bf16_f32 v16, v16, v17
	v_cvt_pk_bf16_f32 v17, v18, v19
	v_cvt_pk_bf16_f32 v18, v8, v9
	v_cvt_pk_bf16_f32 v19, v10, v11
	global_store_dwordx4 v[32:33], v[16:19], off offset:256 sc1
	v_cvt_pk_bf16_f32 v8, v20, v21
	v_cvt_pk_bf16_f32 v9, v22, v23
	v_cvt_pk_bf16_f32 v10, v12, v13
	v_cvt_pk_bf16_f32 v11, v14, v15
	s_nop 1
	v_lshl_add_u64 v[16:17], v[130:131], 0, s[14:15]
	s_mov_b32 s14, 0x58000
	v_add_co_u32_e32 v12, vcc, s14, v130
	s_mov_b64 s[14:15], -1
	s_nop 0
	v_addc_co_u32_e32 v13, vcc, 0, v131, vcc
	global_store_dwordx4 v[12:13], v[8:11], off sc1
	v_cvt_pk_bf16_f32 v4, v4, v5
	v_cvt_pk_bf16_f32 v5, v6, v7
	v_cvt_pk_bf16_f32 v6, v0, v1
	v_cvt_pk_bf16_f32 v7, v2, v3
	global_store_dwordx4 v[16:17], v[4:7], off offset:256 sc1
	s_mov_b32 s99, 1
	s_cbranch_scc1 .LBB0_684
	s_andn2_b64 vcc, exec, s[8:9]
	s_cbranch_vccnz .LBB0_683
	s_barrier
	s_branch .LBB0_683

.LBB0_883:
	s_mov_b32 s99, 0
	s_or_b64 exec, exec, s[38:39]
	v_readlane_b32 s6, v254, 12
	s_waitcnt lgkmcnt(0)
	s_barrier
	s_mov_b32 s59, s70
	s_cmp_eq_u32 s6, 0
	v_mbcnt_lo_u32_b32 v0, -1, 0
	v_mbcnt_hi_u32_b32 v0, -1, v0
	s_barrier
	s_cbranch_scc0 .LBB0_891
	v_and_b32_e32 v0, 63, v0
	v_cmp_gt_u32_e32 vcc, 32, v0
	v_mov_b32_e32 v1, 0
	s_and_saveexec_b64 s[4:5], vcc
	s_cbranch_execz .LBB0_886
	v_readlane_b32 s8, v255, 43
	v_lshlrev_b32_e32 v1, 2, v0
	v_readlane_b32 s9, v255, 44
	s_nop 4
	global_load_dword v1, v1, s[8:9] offset:256 sc1
	s_waitcnt vmcnt(0)
	v_add_u32_e32 v1, 0xff, v1
	v_lshrrev_b32_e32 v1, 8, v1

.LBB0_905:
	s_add_i32 vcc_lo, s24, 2
	s_add_u32 s22, s20, 0x100
	s_addc_u32 s23, s21, 0
	s_add_i32 s62, 0, 0x10000
	s_cmp_eq_u32 s50, s24
	s_cselect_b32 s25, s17, s23
	s_cselect_b32 s24, s16, s22
	v_add_u32_e32 v64, s62, v136
	s_cselect_b32 s27, s19, s87
	s_cselect_b32 s26, s18, s49
	s_add_i32 s63, 0, 0x14000
	ds_read_b128 v[138:141], v64
	ds_read_b128 v[142:145], v64 offset:1024
	ds_read_b128 v[146:149], v64 offset:2048
	ds_read_b128 v[150:153], v64 offset:3072
	v_add_u32_e32 v64, s63, v136
	ds_read_b128 v[154:157], v64
	ds_read_b128 v[158:161], v64 offset:1024
	ds_read_b128 v[162:165], v64 offset:2048
	ds_read_b128 v[166:169], v64 offset:3072
	v_mov_b32_e32 v64, v130
	s_add_u32 s20, s20, s56
	ds_read_b128 v[170:173], v137
	ds_read_b128 v[174:177], v137 offset:1024
	ds_read_b128 v[178:181], v137 offset:2048
	ds_read_b128 v[182:185], v137 offset:3072
	ds_read_b128 v[186:189], v137 offset:4096
	ds_read_b128 v[190:193], v137 offset:5120
	ds_read_b128 v[194:197], v137 offset:6144
	ds_read_b128 v[198:201], v137 offset:7168
	s_addc_u32 s21, s21, s57
	s_add_i32 m0, s30, 0xc000
	s_nop 0
	global_load_lds_dwordx4 v64, s[20:21]
	v_mov_b32_e32 v64, v132
	s_add_i32 m0, s30, 0xe000
	s_nop 0
	global_load_lds_dwordx4 v64, s[20:21]
	s_cmp_eq_u32 s99, 0
	s_cbranch_scc1 .Lrw_d1_n
	s_waitcnt vmcnt(16)
	s_branch .Lrw_d1_d

.Lrw_d1_d:
	s_waitcnt lgkmcnt(0)
	s_barrier
	s_setprio 1
	s_waitcnt lgkmcnt(0)
	v_mfma_f32_16x16x128_f8f6f4 v[126:129], v[138:145], v[170:177], v[126:129]
	v_mfma_f32_16x16x128_f8f6f4 v[122:125], v[146:153], v[170:177], v[122:125]
	v_mfma_f32_16x16x128_f8f6f4 v[110:113], v[138:145], v[178:185], v[110:113]
	v_mfma_f32_16x16x128_f8f6f4 v[106:109], v[146:153], v[178:185], v[106:109]
	v_mfma_f32_16x16x128_f8f6f4 v[202:205], v[138:145], v[186:193], v[94:97]
	v_mfma_f32_16x16x128_f8f6f4 v[206:209], v[146:153], v[186:193], v[90:93]
	v_mfma_f32_16x16x128_f8f6f4 v[210:213], v[138:145], v[194:201], v[78:81]
	v_mfma_f32_16x16x128_f8f6f4 v[214:217], v[146:153], v[194:201], v[74:77]
	s_setprio 0
	s_setprio 1
	v_mfma_f32_16x16x128_f8f6f4 v[118:121], v[154:161], v[170:177], v[118:121]
	v_mfma_f32_16x16x128_f8f6f4 v[114:117], v[162:169], v[170:177], v[114:117]
	v_mfma_f32_16x16x128_f8f6f4 v[102:105], v[154:161], v[178:185], v[102:105]
	v_mfma_f32_16x16x128_f8f6f4 v[98:101], v[162:169], v[178:185], v[98:101]
	v_mfma_f32_16x16x128_f8f6f4 v[170:173], v[154:161], v[186:193], v[86:89]
	v_mfma_f32_16x16x128_f8f6f4 v[174:177], v[162:169], v[186:193], v[82:85]
	v_mfma_f32_16x16x128_f8f6f4 v[178:181], v[154:161], v[194:201], v[70:73]
	v_mfma_f32_16x16x128_f8f6f4 v[182:185], v[162:169], v[194:201], v[66:69]
	s_setprio 0
	s_barrier
	v_mov_b32_e32 v64, v131
	s_add_i32 s20, s62, s28
	s_nop 2
	ds_read_b128 v[66:69], v137 offset:16384
	ds_read_b128 v[70:73], v137 offset:17408
	ds_read_b128 v[74:77], v137 offset:18432
	ds_read_b128 v[78:81], v137 offset:19456
	ds_read_b128 v[82:85], v137 offset:20480
	ds_read_b128 v[86:89], v137 offset:21504
	ds_read_b128 v[90:93], v137 offset:22528
	ds_read_b128 v[94:97], v137 offset:23552
	s_mov_b32 m0, s20
	s_nop 0
	global_load_lds_dwordx4 v64, s[26:27]
	v_mov_b32_e32 v64, v133
	s_add_i32 m0, s20, 0x2000
	s_add_u32 s20, s26, s6
	global_load_lds_dwordx4 v64, s[26:27]
	s_addc_u32 s21, s27, s7
	v_mov_b32_e32 v64, v131
	s_add_i32 s62, s63, s28
	s_mov_b32 m0, s62
	s_nop 0
	global_load_lds_dwordx4 v64, s[20:21]
	v_mov_b32_e32 v64, v133
	s_add_i32 m0, s62, 0x2000
	s_nop 0
	global_load_lds_dwordx4 v64, s[20:21]
	v_mov_b32_e32 v64, v130
	s_mov_b32 m0, s30
	s_nop 0
	global_load_lds_dwordx4 v64, s[24:25]
	v_mov_b32_e32 v64, v132
	s_mov_b32 m0, s31
	s_nop 0
	global_load_lds_dwordx4 v64, s[24:25]
	s_cmp_eq_u32 s99, 0
	s_cbranch_scc1 .Lrw_d2_n
	s_waitcnt vmcnt(16)
	s_branch .Lrw_d2_d

.Lrw_d2_d:
	s_mov_b32 s99, 0
	s_waitcnt lgkmcnt(0)
	s_barrier
	s_setprio 1
	s_waitcnt lgkmcnt(0)
	v_mfma_f32_16x16x128_f8f6f4 v[60:63], v[138:145], v[66:73], v[60:63]
	v_mfma_f32_16x16x128_f8f6f4 v[56:59], v[146:153], v[66:73], v[56:59]
	v_mfma_f32_16x16x128_f8f6f4 v[186:189], v[138:145], v[74:81], v[44:47]
	v_mfma_f32_16x16x128_f8f6f4 v[190:193], v[146:153], v[74:81], v[40:43]
	v_mfma_f32_16x16x128_f8f6f4 v[194:197], v[138:145], v[82:89], v[28:31]
	v_mfma_f32_16x16x128_f8f6f4 v[198:201], v[146:153], v[82:89], v[24:27]
	v_mfma_f32_16x16x128_f8f6f4 v[218:221], v[138:145], v[90:97], v[12:15]
	v_mfma_f32_16x16x128_f8f6f4 v[222:225], v[146:153], v[90:97], v[8:11]
	s_setprio 0
	s_setprio 1
	v_mfma_f32_16x16x128_f8f6f4 v[52:55], v[154:161], v[66:73], v[52:55]
	v_mfma_f32_16x16x128_f8f6f4 v[48:51], v[162:169], v[66:73], v[48:51]
	v_mfma_f32_16x16x128_f8f6f4 v[230:233], v[154:161], v[74:81], v[36:39]
	v_mfma_f32_16x16x128_f8f6f4 v[234:237], v[162:169], v[74:81], v[32:35]
	v_mfma_f32_16x16x128_f8f6f4 v[238:241], v[154:161], v[82:89], v[20:23]
	v_mfma_f32_16x16x128_f8f6f4 v[242:245], v[162:169], v[82:89], v[16:19]
	v_mfma_f32_16x16x128_f8f6f4 v[246:249], v[154:161], v[90:97], v[4:7]
	v_mfma_f32_16x16x128_f8f6f4 v[250:253], v[162:169], v[90:97], v[0:3]
	s_setprio 0
	s_barrier
	s_add_i32 vcc_hi, 0, 0x18000
	v_add_u32_e32 v8, vcc_hi, v136
	s_add_i32 s44, 0, 0x1c000
	s_nop 1
	ds_read_b128 v[0:3], v8
	ds_read_b128 v[4:7], v8 offset:1024
	ds_read_b128 v[16:19], v8 offset:2048
	ds_read_b128 v[20:23], v8 offset:3072
	v_add_u32_e32 v8, s44, v136
	ds_read_b128 v[138:141], v8
	ds_read_b128 v[142:145], v8 offset:1024
	ds_read_b128 v[146:149], v8 offset:2048
	ds_read_b128 v[150:153], v8 offset:3072
	s_add_u32 s62, s24, s6
	v_mov_b32_e32 v64, v130
	s_mov_b32 m0, s34
	ds_read_b128 v[8:11], v137 offset:32768
	ds_read_b128 v[12:15], v137 offset:33792
	ds_read_b128 v[24:27], v137 offset:34816
	ds_read_b128 v[28:31], v137 offset:35840
	ds_read_b128 v[32:35], v137 offset:36864
	ds_read_b128 v[36:39], v137 offset:37888
	ds_read_b128 v[40:43], v137 offset:38912
	ds_read_b128 v[44:47], v137 offset:39936
	s_addc_u32 s63, s25, s7
	s_nop 0
	global_load_lds_dwordx4 v64, s[62:63]
	v_mov_b32_e32 v64, v132
	s_mov_b32 m0, s35
	s_nop 0
	global_load_lds_dwordx4 v64, s[62:63]
	s_waitcnt vmcnt(8)
	s_waitcnt lgkmcnt(0)
	s_barrier
	s_setprio 1
	s_waitcnt lgkmcnt(0)
	v_mfma_f32_16x16x128_f8f6f4 v[126:129], v[0:7], v[8:15], v[126:129]
	v_mfma_f32_16x16x128_f8f6f4 v[122:125], v[16:23], v[8:15], v[122:125]
	v_mfma_f32_16x16x128_f8f6f4 v[110:113], v[0:7], v[24:31], v[110:113]
	v_mfma_f32_16x16x128_f8f6f4 v[106:109], v[16:23], v[24:31], v[106:109]
	v_mfma_f32_16x16x128_f8f6f4 v[94:97], v[0:7], v[32:39], v[202:205]
	v_mfma_f32_16x16x128_f8f6f4 v[90:93], v[16:23], v[32:39], v[206:209]
	v_mfma_f32_16x16x128_f8f6f4 v[78:81], v[0:7], v[40:47], v[210:213]
	v_mfma_f32_16x16x128_f8f6f4 v[74:77], v[16:23], v[40:47], v[214:217]
	s_setprio 0
	s_setprio 1
	v_mfma_f32_16x16x128_f8f6f4 v[118:121], v[138:145], v[8:15], v[118:121]
	v_mfma_f32_16x16x128_f8f6f4 v[114:117], v[146:153], v[8:15], v[114:117]
	v_mfma_f32_16x16x128_f8f6f4 v[102:105], v[138:145], v[24:31], v[102:105]
	v_mfma_f32_16x16x128_f8f6f4 v[98:101], v[146:153], v[24:31], v[98:101]
	v_mfma_f32_16x16x128_f8f6f4 v[86:89], v[138:145], v[32:39], v[170:173]
	v_mfma_f32_16x16x128_f8f6f4 v[82:85], v[146:153], v[32:39], v[174:177]
	v_mfma_f32_16x16x128_f8f6f4 v[70:73], v[138:145], v[40:47], v[178:181]
	v_mfma_f32_16x16x128_f8f6f4 v[66:69], v[146:153], v[40:47], v[182:185]
	s_setprio 0
	s_barrier
	v_mov_b32_e32 v64, v131
	ds_read_b128 v[32:35], v137 offset:49152
	ds_read_b128 v[36:39], v137 offset:50176
	ds_read_b128 v[154:157], v137 offset:51200
	ds_read_b128 v[158:161], v137 offset:52224
	ds_read_b128 v[162:165], v137 offset:53248
	ds_read_b128 v[166:169], v137 offset:54272
	ds_read_b128 v[170:173], v137 offset:55296
	ds_read_b128 v[174:177], v137 offset:56320
	s_add_i32 s62, vcc_hi, s28
	v_lshl_add_u64 v[8:9], s[26:27], 0, v[64:65]
	v_lshl_add_u64 v[8:9], v[8:9], 0, s[80:81]
	s_mov_b32 m0, s62
	v_mov_b32_e32 v64, v133
	global_load_lds_dwordx4 v[8:9], off
	s_add_i32 m0, s62, 0x2000
	v_lshl_add_u64 v[8:9], s[26:27], 0, v[64:65]
	v_lshl_add_u64 v[8:9], v[8:9], 0, s[80:81]
	v_mov_b32_e32 v64, v131
	global_load_lds_dwordx4 v[8:9], off
	s_add_i32 s26, s44, s28
	v_lshl_add_u64 v[8:9], s[20:21], 0, v[64:65]
	v_lshl_add_u64 v[8:9], v[8:9], 0, s[80:81]
	s_mov_b32 m0, s26
	v_mov_b32_e32 v64, v133
	global_load_lds_dwordx4 v[8:9], off
	s_add_i32 m0, s26, 0x2000
	v_lshl_add_u64 v[8:9], s[20:21], 0, v[64:65]
	v_lshl_add_u64 v[8:9], v[8:9], 0, s[80:81]
	v_mov_b32_e32 v64, v130
	global_load_lds_dwordx4 v[8:9], off
	s_mov_b32 m0, s38
	v_lshl_add_u64 v[8:9], s[24:25], 0, v[64:65]
	v_lshl_add_u64 v[8:9], v[8:9], 0, s[80:81]
	v_mov_b32_e32 v64, v132
	global_load_lds_dwordx4 v[8:9], off
	s_mov_b32 m0, s39
	v_lshl_add_u64 v[8:9], s[24:25], 0, v[64:65]
	v_lshl_add_u64 v[8:9], v[8:9], 0, s[80:81]
	global_load_lds_dwordx4 v[8:9], off
	s_waitcnt vmcnt(8)
	s_waitcnt lgkmcnt(0)
	s_barrier
	s_setprio 1
	s_waitcnt lgkmcnt(0)
	v_mfma_f32_16x16x128_f8f6f4 v[60:63], v[0:7], v[32:39], v[60:63]
	v_mfma_f32_16x16x128_f8f6f4 v[56:59], v[16:23], v[32:39], v[56:59]
	v_mfma_f32_16x16x128_f8f6f4 v[44:47], v[0:7], v[154:161], v[186:189]
	v_mfma_f32_16x16x128_f8f6f4 v[40:43], v[16:23], v[154:161], v[190:193]
	v_mfma_f32_16x16x128_f8f6f4 v[28:31], v[0:7], v[162:169], v[194:197]
	v_mfma_f32_16x16x128_f8f6f4 v[24:27], v[16:23], v[162:169], v[198:201]
	v_mfma_f32_16x16x128_f8f6f4 v[12:15], v[0:7], v[170:177], v[218:221]
	v_mfma_f32_16x16x128_f8f6f4 v[8:11], v[16:23], v[170:177], v[222:225]
	s_setprio 0
	s_setprio 1
	v_mfma_f32_16x16x128_f8f6f4 v[52:55], v[138:145], v[32:39], v[52:55]
	v_mfma_f32_16x16x128_f8f6f4 v[48:51], v[146:153], v[32:39], v[48:51]
	v_mfma_f32_16x16x128_f8f6f4 v[36:39], v[138:145], v[154:161], v[230:233]
	v_mfma_f32_16x16x128_f8f6f4 v[32:35], v[146:153], v[154:161], v[234:237]
	v_mfma_f32_16x16x128_f8f6f4 v[20:23], v[138:145], v[162:169], v[238:241]
	v_mfma_f32_16x16x128_f8f6f4 v[16:19], v[146:153], v[162:169], v[242:245]
	v_mfma_f32_16x16x128_f8f6f4 v[4:7], v[138:145], v[170:177], v[246:249]
	v_mfma_f32_16x16x128_f8f6f4 v[0:3], v[146:153], v[170:177], v[250:253]
	s_setprio 0
	s_barrier
	s_add_u32 s49, s49, 0x100
	s_addc_u32 s87, s87, 0
	s_cmp_ge_i32 vcc_lo, s36
	s_mov_b64 s[20:21], s[22:23]
	s_mov_b32 s24, vcc_lo
	s_cbranch_scc0 .LBB0_905
	v_readlane_b32 s44, v254, 2
	s_mov_b32 s63, s45

.LBB0_909:
	s_lshl_b32 s21, s71, 8
	v_mov_b32_e32 v64, v134
	v_mov_b32_e32 v139, v135
	s_and_b32 s21, s21, 0x300
	s_or_b32 s21, s21, s51
	v_mul_f32_e32 v122, 0.5, v122
	v_lshl_add_u32 v138, v64, 4, s21
	v_mul_f32_e32 v64, 0.5, v126
	v_med3_f32 v126, v122, s55, v228
	v_mul_f32_e32 v122, 0.5, v127
	v_med3_f32 v127, v122, s55, v228
	v_mul_f32_e32 v122, 0.5, v123
	v_med3_f32 v141, v122, s55, v228
	v_mul_f32_e32 v122, 0.5, v128
	v_med3_f32 v128, v122, s55, v228
	v_mul_f32_e32 v122, 0.5, v124
	v_mov_b32_e32 v123, v65
	v_med3_f32 v124, v122, s55, v228
	v_mul_f32_e32 v122, 0.5, v129
	v_cvt_pk_fp8_f32 v123, v126, v141
	v_med3_f32 v64, v64, s55, v228
	v_med3_f32 v129, v122, s55, v228
	v_mov_b32_e32 v122, v65
	v_cvt_pk_fp8_f32 v122, v64, v127
	v_mul_f32_e32 v64, 0.5, v125
	v_mul_f32_e32 v114, 0.5, v114
	v_mul_f32_e32 v115, 0.5, v115
	v_med3_f32 v64, v64, s55, v228
	v_med3_f32 v114, v114, s55, v228
	v_med3_f32 v115, v115, s55, v228
	v_mov_b32_e32 v125, v65
	v_cvt_pk_fp8_f32 v123, v124, v64 op_sel:[0,0,1]
	v_mul_f32_e32 v64, 0.5, v118
	v_mul_f32_e32 v118, 0.5, v119
	v_cvt_pk_fp8_f32 v125, v114, v115
	v_med3_f32 v64, v64, s55, v228
	v_med3_f32 v118, v118, s55, v228
	v_mov_b32_e32 v124, v65
	v_mul_f32_e32 v116, 0.5, v116
	v_cvt_pk_fp8_f32 v124, v64, v118
	v_mul_f32_e32 v64, 0.5, v117
	v_med3_f32 v116, v116, s55, v228
	v_med3_f32 v64, v64, s55, v228
	v_mul_f32_e32 v106, 0.5, v106
	v_cvt_pk_fp8_f32 v125, v116, v64 op_sel:[0,0,1]
	v_mul_f32_e32 v64, 0.5, v110
	v_med3_f32 v110, v106, s55, v228
	v_mul_f32_e32 v106, 0.5, v111
	v_med3_f32 v111, v106, s55, v228
	v_mul_f32_e32 v106, 0.5, v107
	v_med3_f32 v116, v106, s55, v228
	v_mul_f32_e32 v106, 0.5, v112
	v_med3_f32 v112, v106, s55, v228
	v_mul_f32_e32 v106, 0.5, v108
	v_mov_b32_e32 v107, v65
	v_med3_f32 v108, v106, s55, v228
	v_mul_f32_e32 v106, 0.5, v113
	v_cvt_pk_fp8_f32 v107, v110, v116
	v_med3_f32 v64, v64, s55, v228
	v_med3_f32 v113, v106, s55, v228
	v_mov_b32_e32 v106, v65
	v_cvt_pk_fp8_f32 v106, v64, v111
	v_mul_f32_e32 v64, 0.5, v109
	v_med3_f32 v64, v64, s55, v228
	v_cvt_pk_fp8_f32 v107, v108, v64 op_sel:[0,0,1]
	v_mul_f32_e32 v64, 0.5, v102
	v_mul_f32_e32 v98, 0.5, v98
	v_mul_f32_e32 v102, 0.5, v103
	v_mul_f32_e32 v99, 0.5, v99
	s_lshl_b32 s20, s29, 8
	v_med3_f32 v64, v64, s55, v228
	v_med3_f32 v98, v98, s55, v228
	v_med3_f32 v102, v102, s55, v228
	v_med3_f32 v99, v99, s55, v228
	v_mov_b32_e32 v108, v65
	v_mov_b32_e32 v109, v65
	s_add_i32 s20, s20, s37
	v_cvt_pk_fp8_f32 v108, v64, v102
	v_cvt_pk_fp8_f32 v109, v98, v99
	v_add_u32_e32 v140, s20, v139
	v_ashrrev_i32_e32 v141, 31, v140
	v_readlane_b32 s20, v254, 42
	v_mul_f32_e32 v103, 0.5, v104
	v_mul_f32_e32 v100, 0.5, v100
	v_mul_f32_e32 v104, 0.5, v105
	v_mul_f32_e32 v64, 0.5, v101
	v_lshlrev_b64 v[114:115], 10, v[140:141]
	v_readlane_b32 s21, v254, 43
	v_med3_f32 v103, v103, s55, v228
	v_med3_f32 v100, v100, s55, v228
	v_med3_f32 v104, v104, s55, v228
	v_med3_f32 v64, v64, s55, v228
	v_ashrrev_i32_e32 v139, 31, v138
	v_lshl_add_u64 v[114:115], s[20:21], 0, v[114:115]
	v_cvt_pk_fp8_f32 v106, v112, v113 op_sel:[0,0,1]
	v_cvt_pk_fp8_f32 v108, v103, v104 op_sel:[0,0,1]
	v_cvt_pk_fp8_f32 v109, v100, v64 op_sel:[0,0,1]
	v_lshl_add_u64 v[114:115], v[114:115], 0, v[138:139]
	s_movk_i32 s20, 0x4000
	v_mul_f32_e32 v90, 0.5, v90
	v_add_co_u32_e32 v98, vcc, s20, v114
	v_mul_f32_e32 v64, 0.5, v94
	v_med3_f32 v94, v90, s55, v228
	v_mul_f32_e32 v90, 0.5, v95
	v_addc_co_u32_e32 v99, vcc, 0, v115, vcc
	v_med3_f32 v95, v90, s55, v228
	v_mul_f32_e32 v90, 0.5, v91
	global_store_dwordx4 v[98:99], v[106:109], off nt sc1
	v_med3_f32 v98, v90, s55, v228
	v_mul_f32_e32 v90, 0.5, v96
	v_med3_f32 v96, v90, s55, v228
	v_mul_f32_e32 v90, 0.5, v92
	v_mov_b32_e32 v91, v65
	v_med3_f32 v92, v90, s55, v228
	v_mul_f32_e32 v90, 0.5, v97
	v_cvt_pk_fp8_f32 v91, v94, v98
	v_med3_f32 v64, v64, s55, v228
	v_med3_f32 v97, v90, s55, v228
	v_mov_b32_e32 v90, v65
	v_cvt_pk_fp8_f32 v90, v64, v95
	v_mul_f32_e32 v64, 0.5, v93
	v_med3_f32 v64, v64, s55, v228
	v_cvt_pk_fp8_f32 v91, v92, v64 op_sel:[0,0,1]
	v_mul_f32_e32 v64, 0.5, v86
	v_mul_f32_e32 v82, 0.5, v82
	v_mul_f32_e32 v86, 0.5, v87
	v_mul_f32_e32 v83, 0.5, v83
	v_med3_f32 v64, v64, s55, v228
	v_med3_f32 v82, v82, s55, v228
	v_med3_f32 v86, v86, s55, v228
	v_med3_f32 v83, v83, s55, v228
	v_mov_b32_e32 v92, v65
	v_mov_b32_e32 v93, v65
	v_cvt_pk_fp8_f32 v92, v64, v86
	v_cvt_pk_fp8_f32 v93, v82, v83
	v_mul_f32_e32 v87, 0.5, v88
	v_mul_f32_e32 v84, 0.5, v84
	v_mul_f32_e32 v88, 0.5, v89
	v_mul_f32_e32 v64, 0.5, v85
	v_med3_f32 v87, v87, s55, v228
	v_med3_f32 v84, v84, s55, v228
	v_med3_f32 v88, v88, s55, v228
	v_med3_f32 v64, v64, s55, v228
	v_cvt_pk_fp8_f32 v90, v96, v97 op_sel:[0,0,1]
	v_cvt_pk_fp8_f32 v92, v87, v88 op_sel:[0,0,1]
	v_cvt_pk_fp8_f32 v93, v84, v64 op_sel:[0,0,1]
	s_mov_b32 s20, 0x8000
	v_mul_f32_e32 v74, 0.5, v74
	v_add_co_u32_e32 v82, vcc, s20, v114
	v_mul_f32_e32 v64, 0.5, v78
	v_med3_f32 v78, v74, s55, v228
	v_mul_f32_e32 v74, 0.5, v79
	v_addc_co_u32_e32 v83, vcc, 0, v115, vcc
	v_med3_f32 v79, v74, s55, v228
	v_mul_f32_e32 v74, 0.5, v75
	global_store_dwordx4 v[82:83], v[90:93], off nt sc1
	v_med3_f32 v82, v74, s55, v228
	v_mul_f32_e32 v74, 0.5, v80
	v_med3_f32 v80, v74, s55, v228
	v_mul_f32_e32 v74, 0.5, v76
	v_mov_b32_e32 v75, v65
	v_med3_f32 v76, v74, s55, v228
	v_mul_f32_e32 v74, 0.5, v81
	v_cvt_pk_fp8_f32 v75, v78, v82
	v_med3_f32 v64, v64, s55, v228
	v_med3_f32 v81, v74, s55, v228
	v_mov_b32_e32 v74, v65
	v_cvt_pk_fp8_f32 v74, v64, v79
	v_mul_f32_e32 v64, 0.5, v77
	v_med3_f32 v64, v64, s55, v228
	v_cvt_pk_fp8_f32 v75, v76, v64 op_sel:[0,0,1]
	v_mul_f32_e32 v64, 0.5, v70
	v_mul_f32_e32 v66, 0.5, v66
	v_mul_f32_e32 v70, 0.5, v71
	v_mul_f32_e32 v67, 0.5, v67
	v_med3_f32 v64, v64, s55, v228
	v_med3_f32 v66, v66, s55, v228
	v_med3_f32 v70, v70, s55, v228
	v_med3_f32 v67, v67, s55, v228
	v_mov_b32_e32 v76, v65
	v_mov_b32_e32 v77, v65
	v_cvt_pk_fp8_f32 v76, v64, v70
	v_cvt_pk_fp8_f32 v77, v66, v67
	v_mul_f32_e32 v71, 0.5, v72
	v_mul_f32_e32 v68, 0.5, v68
	v_mul_f32_e32 v72, 0.5, v73
	v_mul_f32_e32 v64, 0.5, v69
	v_med3_f32 v71, v71, s55, v228
	v_med3_f32 v68, v68, s55, v228
	v_med3_f32 v72, v72, s55, v228
	v_med3_f32 v64, v64, s55, v228
	v_cvt_pk_fp8_f32 v74, v80, v81 op_sel:[0,0,1]
	v_cvt_pk_fp8_f32 v76, v71, v72 op_sel:[0,0,1]
	v_cvt_pk_fp8_f32 v77, v68, v64 op_sel:[0,0,1]
	s_mov_b32 s20, 0xc000
	v_mul_f32_e32 v56, 0.5, v56
	v_add_co_u32_e32 v66, vcc, s20, v114
	v_med3_f32 v64, v56, s55, v228
	v_mul_f32_e32 v56, 0.5, v61
	v_addc_co_u32_e32 v67, vcc, 0, v115, vcc
	v_med3_f32 v61, v56, s55, v228
	v_mul_f32_e32 v56, 0.5, v57
	global_store_dwordx4 v[66:67], v[74:77], off nt sc1
	v_med3_f32 v66, v56, s55, v228
	v_mov_b32_e32 v57, v65
	v_cvt_pk_fp8_f32 v57, v64, v66
	v_mul_f32_e32 v56, 0.5, v62
	v_med3_f32 v62, v56, s55, v228
	v_mul_f32_e32 v56, 0.5, v58
	v_mul_f32_e32 v59, 0.5, v59
	v_mul_f32_e32 v60, 0.5, v60
	v_med3_f32 v58, v56, s55, v228
	v_mul_f32_e32 v56, 0.5, v63
	v_med3_f32 v59, v59, s55, v228
	v_mul_f32_e32 v52, 0.5, v52
	v_mul_f32_e32 v48, 0.5, v48
	v_mul_f32_e32 v53, 0.5, v53
	v_mul_f32_e32 v49, 0.5, v49
	v_med3_f32 v60, v60, s55, v228
	v_med3_f32 v63, v56, s55, v228
	v_mov_b32_e32 v56, v65
	v_cvt_pk_fp8_f32 v57, v58, v59 op_sel:[0,0,1]
	v_med3_f32 v52, v52, s55, v228
	v_med3_f32 v48, v48, s55, v228
	v_med3_f32 v53, v53, s55, v228
	v_med3_f32 v49, v49, s55, v228
	v_mov_b32_e32 v58, v65
	v_mov_b32_e32 v59, v65
	v_cvt_pk_fp8_f32 v56, v60, v61
	v_cvt_pk_fp8_f32 v58, v52, v53
	v_cvt_pk_fp8_f32 v59, v48, v49
	v_mul_f32_e32 v54, 0.5, v54
	v_mul_f32_e32 v50, 0.5, v50
	v_mul_f32_e32 v55, 0.5, v55
	v_mul_f32_e32 v48, 0.5, v51
	v_med3_f32 v54, v54, s55, v228
	v_med3_f32 v50, v50, s55, v228
	v_med3_f32 v55, v55, s55, v228
	v_med3_f32 v48, v48, s55, v228
	v_cvt_pk_fp8_f32 v56, v62, v63 op_sel:[0,0,1]
	v_cvt_pk_fp8_f32 v58, v54, v55 op_sel:[0,0,1]
	v_cvt_pk_fp8_f32 v59, v50, v48 op_sel:[0,0,1]
	s_mov_b32 s20, 0x20000
	v_add_co_u32_e32 v48, vcc, s20, v114
	v_mul_f32_e32 v40, 0.5, v40
	s_nop 0
	v_addc_co_u32_e32 v49, vcc, 0, v115, vcc
	global_store_dwordx4 v[48:49], v[56:59], off nt sc1
	v_med3_f32 v48, v40, s55, v228
	v_mul_f32_e32 v40, 0.5, v45
	v_med3_f32 v45, v40, s55, v228
	v_mul_f32_e32 v40, 0.5, v41
	v_med3_f32 v49, v40, s55, v228
	v_mov_b32_e32 v41, v65
	v_cvt_pk_fp8_f32 v41, v48, v49
	v_mul_f32_e32 v40, 0.5, v46
	v_med3_f32 v46, v40, s55, v228
	v_mul_f32_e32 v40, 0.5, v42
	v_mul_f32_e32 v43, 0.5, v43
	v_mul_f32_e32 v44, 0.5, v44
	v_med3_f32 v42, v40, s55, v228
	v_mul_f32_e32 v40, 0.5, v47
	v_med3_f32 v43, v43, s55, v228
	v_mul_f32_e32 v36, 0.5, v36
	v_mul_f32_e32 v32, 0.5, v32
	v_mul_f32_e32 v37, 0.5, v37
	v_mul_f32_e32 v33, 0.5, v33
	v_med3_f32 v44, v44, s55, v228
	v_med3_f32 v47, v40, s55, v228
	v_mov_b32_e32 v40, v65
	v_cvt_pk_fp8_f32 v41, v42, v43 op_sel:[0,0,1]
	v_med3_f32 v36, v36, s55, v228
	v_med3_f32 v32, v32, s55, v228
	v_med3_f32 v37, v37, s55, v228
	v_med3_f32 v33, v33, s55, v228
	v_mov_b32_e32 v42, v65
	v_mov_b32_e32 v43, v65
	v_cvt_pk_fp8_f32 v40, v44, v45
	v_cvt_pk_fp8_f32 v42, v36, v37
	v_cvt_pk_fp8_f32 v43, v32, v33
	v_mul_f32_e32 v38, 0.5, v38
	v_mul_f32_e32 v34, 0.5, v34
	v_mul_f32_e32 v39, 0.5, v39
	v_mul_f32_e32 v32, 0.5, v35
	v_med3_f32 v38, v38, s55, v228
	v_med3_f32 v34, v34, s55, v228
	v_med3_f32 v39, v39, s55, v228
	v_med3_f32 v32, v32, s55, v228
	v_cvt_pk_fp8_f32 v40, v46, v47 op_sel:[0,0,1]
	v_cvt_pk_fp8_f32 v42, v38, v39 op_sel:[0,0,1]
	v_cvt_pk_fp8_f32 v43, v34, v32 op_sel:[0,0,1]
	s_mov_b32 s20, 0x24000
	v_add_co_u32_e32 v32, vcc, s20, v114
	v_mul_f32_e32 v24, 0.5, v24
	s_nop 0
	v_addc_co_u32_e32 v33, vcc, 0, v115, vcc
	global_store_dwordx4 v[32:33], v[40:43], off nt sc1
	v_med3_f32 v32, v24, s55, v228
	v_mul_f32_e32 v24, 0.5, v29
	v_med3_f32 v29, v24, s55, v228
	v_mul_f32_e32 v24, 0.5, v25
	v_med3_f32 v33, v24, s55, v228
	v_mov_b32_e32 v25, v65
	v_cvt_pk_fp8_f32 v25, v32, v33
	v_mul_f32_e32 v24, 0.5, v30
	v_med3_f32 v30, v24, s55, v228
	v_mul_f32_e32 v24, 0.5, v26
	v_mul_f32_e32 v27, 0.5, v27
	v_mul_f32_e32 v28, 0.5, v28
	v_med3_f32 v26, v24, s55, v228
	v_mul_f32_e32 v24, 0.5, v31
	v_med3_f32 v27, v27, s55, v228
	v_mul_f32_e32 v20, 0.5, v20
	v_mul_f32_e32 v16, 0.5, v16
	v_mul_f32_e32 v21, 0.5, v21
	v_mul_f32_e32 v17, 0.5, v17
	v_med3_f32 v28, v28, s55, v228
	v_med3_f32 v31, v24, s55, v228
	v_mov_b32_e32 v24, v65
	v_cvt_pk_fp8_f32 v25, v26, v27 op_sel:[0,0,1]
	v_med3_f32 v20, v20, s55, v228
	v_med3_f32 v16, v16, s55, v228
	v_med3_f32 v21, v21, s55, v228
	v_med3_f32 v17, v17, s55, v228
	v_mov_b32_e32 v26, v65
	v_mov_b32_e32 v27, v65
	v_cvt_pk_fp8_f32 v24, v28, v29
	v_cvt_pk_fp8_f32 v26, v20, v21
	v_cvt_pk_fp8_f32 v27, v16, v17
	v_mul_f32_e32 v22, 0.5, v22
	v_mul_f32_e32 v18, 0.5, v18
	v_mul_f32_e32 v23, 0.5, v23
	v_mul_f32_e32 v16, 0.5, v19
	v_med3_f32 v22, v22, s55, v228
	v_med3_f32 v18, v18, s55, v228
	v_med3_f32 v23, v23, s55, v228
	v_med3_f32 v16, v16, s55, v228
	v_cvt_pk_fp8_f32 v24, v30, v31 op_sel:[0,0,1]
	v_cvt_pk_fp8_f32 v26, v22, v23 op_sel:[0,0,1]
	v_cvt_pk_fp8_f32 v27, v18, v16 op_sel:[0,0,1]
	s_mov_b32 s20, 0x28000
	v_add_co_u32_e32 v16, vcc, s20, v114
	v_mul_f32_e32 v8, 0.5, v8
	s_nop 0
	v_addc_co_u32_e32 v17, vcc, 0, v115, vcc
	global_store_dwordx4 v[16:17], v[24:27], off nt sc1
	v_med3_f32 v16, v8, s55, v228
	v_mul_f32_e32 v8, 0.5, v13
	v_med3_f32 v13, v8, s55, v228
	v_mul_f32_e32 v8, 0.5, v9
	v_med3_f32 v17, v8, s55, v228
	v_mov_b32_e32 v9, v65
	v_cvt_pk_fp8_f32 v9, v16, v17
	v_mul_f32_e32 v8, 0.5, v14
	v_med3_f32 v14, v8, s55, v228
	v_mul_f32_e32 v8, 0.5, v10
	v_mul_f32_e32 v11, 0.5, v11
	v_mul_f32_e32 v12, 0.5, v12
	v_med3_f32 v10, v8, s55, v228
	v_mul_f32_e32 v8, 0.5, v15
	v_med3_f32 v11, v11, s55, v228
	v_mul_f32_e32 v4, 0.5, v4
	v_mul_f32_e32 v0, 0.5, v0
	v_mul_f32_e32 v5, 0.5, v5
	v_mul_f32_e32 v1, 0.5, v1
	v_med3_f32 v12, v12, s55, v228
	v_med3_f32 v15, v8, s55, v228
	v_mov_b32_e32 v8, v65
	v_cvt_pk_fp8_f32 v9, v10, v11 op_sel:[0,0,1]
	v_med3_f32 v4, v4, s55, v228
	v_med3_f32 v0, v0, s55, v228
	v_med3_f32 v5, v5, s55, v228
	v_med3_f32 v1, v1, s55, v228
	v_mov_b32_e32 v10, v65
	v_mov_b32_e32 v11, v65
	v_cvt_pk_fp8_f32 v8, v12, v13
	v_cvt_pk_fp8_f32 v10, v4, v5
	v_cvt_pk_fp8_f32 v11, v0, v1
	v_mul_f32_e32 v119, 0.5, v120
	v_mul_f32_e32 v120, 0.5, v121
	v_mul_f32_e32 v6, 0.5, v6
	v_mul_f32_e32 v2, 0.5, v2
	v_mul_f32_e32 v7, 0.5, v7
	v_mul_f32_e32 v0, 0.5, v3
	v_med3_f32 v119, v119, s55, v228
	v_med3_f32 v120, v120, s55, v228
	v_med3_f32 v6, v6, s55, v228
	v_med3_f32 v2, v2, s55, v228
	v_med3_f32 v7, v7, s55, v228
	v_med3_f32 v0, v0, s55, v228
	v_cvt_pk_fp8_f32 v122, v128, v129 op_sel:[0,0,1]
	v_cvt_pk_fp8_f32 v124, v119, v120 op_sel:[0,0,1]
	v_cvt_pk_fp8_f32 v8, v14, v15 op_sel:[0,0,1]
	v_cvt_pk_fp8_f32 v10, v6, v7 op_sel:[0,0,1]
	v_cvt_pk_fp8_f32 v11, v2, v0 op_sel:[0,0,1]
	v_add_co_u32_e32 v0, vcc, 0x2c000, v114
	global_store_dwordx4 v[114:115], v[122:125], off nt sc1
	s_nop 0
	v_addc_co_u32_e32 v1, vcc, 0, v115, vcc
	s_and_b64 vcc, exec, s[4:5]
	s_mov_b64 s[4:5], -1
	global_store_dwordx4 v[0:1], v[8:11], off nt sc1
	s_mov_b32 s99, 1
	s_cbranch_vccnz .LBB0_896
	s_andn2_b64 vcc, exec, s[10:11]
	s_cbranch_vccnz .LBB0_895
	s_barrier
	s_branch .LBB0_895
